# v9 + K-loop staging loads use the SGPR tile base plus the 32-bit per-lane offset directly (global_load_lds saddr form): 15-16 64-bit VALU adds per two K-tiles removed, one address VGPR per load instea
# baseline (speedup 1.0000x reference)
.LBB0_171:
	s_add_u32 s16, s62, 0x4000
	s_addc_u32 s17, s63, 0
	s_cmp_eq_u32 vcc_hi, 28
	s_cselect_b32 s68, s29, s16
	s_cselect_b32 s69, s15, s17
	s_cselect_b32 s67, s53, vcc_lo
	s_cselect_b32 s66, s55, s61
	s_add_u32 s64, s68, 0x8000
	s_addc_u32 s65, s69, 0
	s_add_i32 s16, 0, 0x10000
	s_add_i32 s17, 0, 0x14000
	v_add_u32_e32 v94, s16, v182
	v_add_u32_e32 v114, s17, v182
	ds_read_b128 v[82:85], v94
	ds_read_b128 v[86:89], v94 offset:1024
	ds_read_b128 v[90:93], v94 offset:2048
	ds_read_b128 v[94:97], v94 offset:3072
	ds_read_b128 v[174:177], v114
	ds_read_b128 v[178:181], v114 offset:1024
	ds_read_b128 v[214:217], v114 offset:2048
	ds_read_b128 v[218:221], v114 offset:3072
	s_add_i32 m0, s37, 0xc000
	ds_read_b128 v[222:225], v212
	ds_read_b128 v[226:229], v212 offset:1024
	ds_read_b128 v[230:233], v212 offset:2048
	ds_read_b128 v[234:237], v212 offset:3072
	ds_read_b128 v[238:241], v212 offset:4096
	ds_read_b128 v[242:245], v212 offset:5120
	ds_read_b128 v[246:249], v212 offset:6144
	ds_read_b128 v[250:253], v212 offset:7168
	global_load_lds_dwordx4 v170, s[62:63]
	s_add_i32 m0, s37, 0xe000
	s_nop 0
	global_load_lds_dwordx4 v172, s[62:63]
	s_waitcnt vmcnt(8)
	s_waitcnt lgkmcnt(0)
	s_barrier
	s_setprio 1
	s_waitcnt lgkmcnt(0)
	v_mfma_f32_16x16x32_bf16 v[144:147], v[82:85], v[222:225], v[144:147]
	v_mfma_f32_16x16x32_bf16 v[140:143], v[90:93], v[222:225], v[140:143]
	v_mfma_f32_16x16x32_bf16 v[128:131], v[82:85], v[230:233], v[128:131]
	v_mfma_f32_16x16x32_bf16 v[124:127], v[90:93], v[230:233], v[124:127]
	v_mfma_f32_16x16x32_bf16 v[110:113], v[82:85], v[238:241], v[110:113]
	v_mfma_f32_16x16x32_bf16 v[106:109], v[90:93], v[238:241], v[106:109]
	v_mfma_f32_16x16x32_bf16 v[78:81], v[82:85], v[246:249], v[78:81]
	v_mfma_f32_16x16x32_bf16 v[74:77], v[90:93], v[246:249], v[74:77]
	v_mfma_f32_16x16x32_bf16 v[144:147], v[86:89], v[226:229], v[144:147]
	v_mfma_f32_16x16x32_bf16 v[140:143], v[94:97], v[226:229], v[140:143]
	v_mfma_f32_16x16x32_bf16 v[128:131], v[86:89], v[234:237], v[128:131]
	v_mfma_f32_16x16x32_bf16 v[124:127], v[94:97], v[234:237], v[124:127]
	v_mfma_f32_16x16x32_bf16 v[110:113], v[86:89], v[242:245], v[110:113]
	v_mfma_f32_16x16x32_bf16 v[106:109], v[94:97], v[242:245], v[106:109]
	v_mfma_f32_16x16x32_bf16 v[78:81], v[86:89], v[250:253], v[78:81]
	v_mfma_f32_16x16x32_bf16 v[74:77], v[94:97], v[250:253], v[74:77]
	s_setprio 0
	s_setprio 1
	v_mfma_f32_16x16x32_bf16 v[136:139], v[174:177], v[222:225], v[136:139]
	v_mfma_f32_16x16x32_bf16 v[132:135], v[214:217], v[222:225], v[132:135]
	v_mfma_f32_16x16x32_bf16 v[120:123], v[174:177], v[230:233], v[120:123]
	v_mfma_f32_16x16x32_bf16 v[116:119], v[214:217], v[230:233], v[116:119]
	v_mfma_f32_16x16x32_bf16 v[102:105], v[174:177], v[238:241], v[102:105]
	v_mfma_f32_16x16x32_bf16 v[98:101], v[214:217], v[238:241], v[98:101]
	v_mfma_f32_16x16x32_bf16 v[70:73], v[174:177], v[246:249], v[70:73]
	v_mfma_f32_16x16x32_bf16 v[66:69], v[214:217], v[246:249], v[66:69]
	v_mfma_f32_16x16x32_bf16 v[136:139], v[178:181], v[226:229], v[136:139]
	v_mfma_f32_16x16x32_bf16 v[132:135], v[218:221], v[226:229], v[132:135]
	v_mfma_f32_16x16x32_bf16 v[120:123], v[178:181], v[234:237], v[120:123]
	v_mfma_f32_16x16x32_bf16 v[116:119], v[218:221], v[234:237], v[116:119]
	v_mfma_f32_16x16x32_bf16 v[102:105], v[178:181], v[242:245], v[102:105]
	v_mfma_f32_16x16x32_bf16 v[98:101], v[218:221], v[242:245], v[98:101]
	v_mfma_f32_16x16x32_bf16 v[70:73], v[178:181], v[250:253], v[70:73]
	v_mfma_f32_16x16x32_bf16 v[66:69], v[218:221], v[250:253], v[66:69]
	s_setprio 0
	s_barrier
	s_add_i32 s16, s16, s9
	s_mov_b32 m0, s16
	ds_read_b128 v[222:225], v212 offset:16384
	ds_read_b128 v[226:229], v212 offset:17408
	ds_read_b128 v[230:233], v212 offset:18432
	ds_read_b128 v[234:237], v212 offset:19456
	ds_read_b128 v[238:241], v212 offset:20480
	ds_read_b128 v[242:245], v212 offset:21504
	ds_read_b128 v[246:249], v212 offset:22528
	ds_read_b128 v[250:253], v212 offset:23552
	global_load_lds_dwordx4 v150, s[66:67]
	s_add_i32 m0, s16, 0x2000
	s_add_u32 s26, s66, 0x1000
	s_addc_u32 s27, s67, 0
	s_add_i32 s16, s17, s9
	global_load_lds_dwordx4 v154, s[66:67]
	s_mov_b32 m0, s16
	s_nop 0
	global_load_lds_dwordx4 v150, s[26:27]
	s_add_i32 m0, s16, 0x2000
	s_nop 0
	global_load_lds_dwordx4 v154, s[26:27]
	s_mov_b32 m0, s37
	s_nop 0
	global_load_lds_dwordx4 v148, s[68:69]
	s_mov_b32 m0, s70
	s_nop 0
	global_load_lds_dwordx4 v152, s[68:69]
	s_waitcnt vmcnt(8)
	s_waitcnt lgkmcnt(0)
	s_barrier
	s_setprio 1
	s_waitcnt lgkmcnt(0)
	v_mfma_f32_16x16x32_bf16 v[62:65], v[82:85], v[222:225], v[62:65]
	v_mfma_f32_16x16x32_bf16 v[58:61], v[90:93], v[222:225], v[58:61]
	v_mfma_f32_16x16x32_bf16 v[46:49], v[82:85], v[230:233], v[46:49]
	v_mfma_f32_16x16x32_bf16 v[42:45], v[90:93], v[230:233], v[42:45]
	v_mfma_f32_16x16x32_bf16 v[30:33], v[82:85], v[238:241], v[30:33]
	v_mfma_f32_16x16x32_bf16 v[26:29], v[90:93], v[238:241], v[26:29]
	v_mfma_f32_16x16x32_bf16 v[14:17], v[82:85], v[246:249], v[14:17]
	v_mfma_f32_16x16x32_bf16 v[10:13], v[90:93], v[246:249], v[10:13]
	v_mfma_f32_16x16x32_bf16 v[62:65], v[86:89], v[226:229], v[62:65]
	v_mfma_f32_16x16x32_bf16 v[58:61], v[94:97], v[226:229], v[58:61]
	v_mfma_f32_16x16x32_bf16 v[46:49], v[86:89], v[234:237], v[46:49]
	v_mfma_f32_16x16x32_bf16 v[42:45], v[94:97], v[234:237], v[42:45]
	v_mfma_f32_16x16x32_bf16 v[30:33], v[86:89], v[242:245], v[30:33]
	v_mfma_f32_16x16x32_bf16 v[26:29], v[94:97], v[242:245], v[26:29]
	v_mfma_f32_16x16x32_bf16 v[14:17], v[86:89], v[250:253], v[14:17]
	v_mfma_f32_16x16x32_bf16 v[10:13], v[94:97], v[250:253], v[10:13]
	s_setprio 0
	s_setprio 1
	v_mfma_f32_16x16x32_bf16 v[54:57], v[174:177], v[222:225], v[54:57]
	v_mfma_f32_16x16x32_bf16 v[50:53], v[214:217], v[222:225], v[50:53]
	v_mfma_f32_16x16x32_bf16 v[38:41], v[174:177], v[230:233], v[38:41]
	v_mfma_f32_16x16x32_bf16 v[34:37], v[214:217], v[230:233], v[34:37]
	v_mfma_f32_16x16x32_bf16 v[22:25], v[174:177], v[238:241], v[22:25]
	v_mfma_f32_16x16x32_bf16 v[18:21], v[214:217], v[238:241], v[18:21]
	v_mfma_f32_16x16x32_bf16 v[6:9], v[174:177], v[246:249], v[6:9]
	v_mfma_f32_16x16x32_bf16 v[2:5], v[214:217], v[246:249], v[2:5]
	v_mfma_f32_16x16x32_bf16 v[54:57], v[178:181], v[226:229], v[54:57]
	v_mfma_f32_16x16x32_bf16 v[50:53], v[218:221], v[226:229], v[50:53]
	v_mfma_f32_16x16x32_bf16 v[38:41], v[178:181], v[234:237], v[38:41]
	v_mfma_f32_16x16x32_bf16 v[34:37], v[218:221], v[234:237], v[34:37]
	v_mfma_f32_16x16x32_bf16 v[22:25], v[178:181], v[242:245], v[22:25]
	v_mfma_f32_16x16x32_bf16 v[18:21], v[218:221], v[242:245], v[18:21]
	v_mfma_f32_16x16x32_bf16 v[6:9], v[178:181], v[250:253], v[6:9]
	v_mfma_f32_16x16x32_bf16 v[2:5], v[218:221], v[250:253], v[2:5]
	s_setprio 0
	s_barrier
	s_add_i32 s16, 0, 0x18000
	s_add_i32 s17, 0, 0x1c000
	v_add_u32_e32 v94, s16, v182
	v_add_u32_e32 v114, s17, v182
	ds_read_b128 v[82:85], v94
	ds_read_b128 v[86:89], v94 offset:1024
	ds_read_b128 v[90:93], v94 offset:2048
	ds_read_b128 v[94:97], v94 offset:3072
	ds_read_b128 v[174:177], v114
	ds_read_b128 v[178:181], v114 offset:1024
	ds_read_b128 v[214:217], v114 offset:2048
	ds_read_b128 v[218:221], v114 offset:3072
	s_add_u32 s26, s68, 0x4000
	s_addc_u32 s27, s69, 0
	s_mov_b32 m0, s71
	ds_read_b128 v[222:225], v212 offset:32768
	ds_read_b128 v[226:229], v212 offset:33792
	ds_read_b128 v[230:233], v212 offset:34816
	ds_read_b128 v[234:237], v212 offset:35840
	ds_read_b128 v[238:241], v212 offset:36864
	ds_read_b128 v[242:245], v212 offset:37888
	ds_read_b128 v[246:249], v212 offset:38912
	ds_read_b128 v[250:253], v212 offset:39936
	global_load_lds_dwordx4 v148, s[26:27]
	s_mov_b32 m0, s74
	s_nop 0
	global_load_lds_dwordx4 v152, s[26:27]
	s_waitcnt vmcnt(8)
	s_waitcnt lgkmcnt(0)
	s_barrier
	s_setprio 1
	s_waitcnt lgkmcnt(0)
	v_mfma_f32_16x16x32_bf16 v[144:147], v[82:85], v[222:225], v[144:147]
	v_mfma_f32_16x16x32_bf16 v[140:143], v[90:93], v[222:225], v[140:143]
	v_mfma_f32_16x16x32_bf16 v[128:131], v[82:85], v[230:233], v[128:131]
	v_mfma_f32_16x16x32_bf16 v[124:127], v[90:93], v[230:233], v[124:127]
	v_mfma_f32_16x16x32_bf16 v[110:113], v[82:85], v[238:241], v[110:113]
	v_mfma_f32_16x16x32_bf16 v[106:109], v[90:93], v[238:241], v[106:109]
	v_mfma_f32_16x16x32_bf16 v[78:81], v[82:85], v[246:249], v[78:81]
	v_mfma_f32_16x16x32_bf16 v[74:77], v[90:93], v[246:249], v[74:77]
	v_mfma_f32_16x16x32_bf16 v[144:147], v[86:89], v[226:229], v[144:147]
	v_mfma_f32_16x16x32_bf16 v[140:143], v[94:97], v[226:229], v[140:143]
	v_mfma_f32_16x16x32_bf16 v[128:131], v[86:89], v[234:237], v[128:131]
	v_mfma_f32_16x16x32_bf16 v[124:127], v[94:97], v[234:237], v[124:127]
	v_mfma_f32_16x16x32_bf16 v[110:113], v[86:89], v[242:245], v[110:113]
	v_mfma_f32_16x16x32_bf16 v[106:109], v[94:97], v[242:245], v[106:109]
	v_mfma_f32_16x16x32_bf16 v[78:81], v[86:89], v[250:253], v[78:81]
	v_mfma_f32_16x16x32_bf16 v[74:77], v[94:97], v[250:253], v[74:77]
	s_setprio 0
	s_setprio 1
	v_mfma_f32_16x16x32_bf16 v[136:139], v[174:177], v[222:225], v[136:139]
	v_mfma_f32_16x16x32_bf16 v[132:135], v[214:217], v[222:225], v[132:135]
	v_mfma_f32_16x16x32_bf16 v[120:123], v[174:177], v[230:233], v[120:123]
	v_mfma_f32_16x16x32_bf16 v[116:119], v[214:217], v[230:233], v[116:119]
	v_mfma_f32_16x16x32_bf16 v[102:105], v[174:177], v[238:241], v[102:105]
	v_mfma_f32_16x16x32_bf16 v[98:101], v[214:217], v[238:241], v[98:101]
	v_mfma_f32_16x16x32_bf16 v[70:73], v[174:177], v[246:249], v[70:73]
	v_mfma_f32_16x16x32_bf16 v[66:69], v[214:217], v[246:249], v[66:69]
	v_mfma_f32_16x16x32_bf16 v[136:139], v[178:181], v[226:229], v[136:139]
	v_mfma_f32_16x16x32_bf16 v[132:135], v[218:221], v[226:229], v[132:135]
	v_mfma_f32_16x16x32_bf16 v[120:123], v[178:181], v[234:237], v[120:123]
	v_mfma_f32_16x16x32_bf16 v[116:119], v[218:221], v[234:237], v[116:119]
	v_mfma_f32_16x16x32_bf16 v[102:105], v[178:181], v[242:245], v[102:105]
	v_mfma_f32_16x16x32_bf16 v[98:101], v[218:221], v[242:245], v[98:101]
	v_mfma_f32_16x16x32_bf16 v[70:73], v[178:181], v[250:253], v[70:73]
	v_mfma_f32_16x16x32_bf16 v[66:69], v[218:221], v[250:253], v[66:69]
	s_setprio 0
	s_barrier
	s_add_u32 s26, s66, 0x8000
	s_addc_u32 s27, s67, 0
	s_add_i32 s16, s16, s9
	s_mov_b32 m0, s16
	ds_read_b128 v[222:225], v212 offset:49152
	ds_read_b128 v[226:229], v212 offset:50176
	ds_read_b128 v[230:233], v212 offset:51200
	ds_read_b128 v[234:237], v212 offset:52224
	ds_read_b128 v[238:241], v212 offset:53248
	ds_read_b128 v[242:245], v212 offset:54272
	ds_read_b128 v[246:249], v212 offset:55296
	ds_read_b128 v[250:253], v212 offset:56320
	global_load_lds_dwordx4 v150, s[26:27]
	s_add_i32 m0, s16, 0x2000
	v_lshl_add_u64 v[158:159], s[26:27], 0, v[154:155]
	s_add_u32 s26, s66, 0x9000
	s_addc_u32 s27, s67, 0
	s_add_i32 s16, s17, s9
	global_load_lds_dwordx4 v[158:159], off
	s_mov_b32 m0, s16
	s_nop 0
	global_load_lds_dwordx4 v150, s[26:27]
	s_add_i32 m0, s16, 0x2000
	s_nop 0
	global_load_lds_dwordx4 v154, s[26:27]
	s_mov_b32 m0, s86
	s_nop 0
	global_load_lds_dwordx4 v148, s[64:65]
	s_mov_b32 m0, s87
	s_nop 0
	global_load_lds_dwordx4 v152, s[64:65]
	s_waitcnt vmcnt(8)
	s_waitcnt lgkmcnt(0)
	s_barrier
	s_setprio 1
	s_waitcnt lgkmcnt(0)
	v_mfma_f32_16x16x32_bf16 v[62:65], v[82:85], v[222:225], v[62:65]
	v_mfma_f32_16x16x32_bf16 v[58:61], v[90:93], v[222:225], v[58:61]
	v_mfma_f32_16x16x32_bf16 v[46:49], v[82:85], v[230:233], v[46:49]
	v_mfma_f32_16x16x32_bf16 v[42:45], v[90:93], v[230:233], v[42:45]
	v_mfma_f32_16x16x32_bf16 v[30:33], v[82:85], v[238:241], v[30:33]
	v_mfma_f32_16x16x32_bf16 v[26:29], v[90:93], v[238:241], v[26:29]
	v_mfma_f32_16x16x32_bf16 v[14:17], v[82:85], v[246:249], v[14:17]
	v_mfma_f32_16x16x32_bf16 v[10:13], v[90:93], v[246:249], v[10:13]
	v_mfma_f32_16x16x32_bf16 v[62:65], v[86:89], v[226:229], v[62:65]
	v_mfma_f32_16x16x32_bf16 v[58:61], v[94:97], v[226:229], v[58:61]
	v_mfma_f32_16x16x32_bf16 v[46:49], v[86:89], v[234:237], v[46:49]
	v_mfma_f32_16x16x32_bf16 v[42:45], v[94:97], v[234:237], v[42:45]
	v_mfma_f32_16x16x32_bf16 v[30:33], v[86:89], v[242:245], v[30:33]
	v_mfma_f32_16x16x32_bf16 v[26:29], v[94:97], v[242:245], v[26:29]
	v_mfma_f32_16x16x32_bf16 v[14:17], v[86:89], v[250:253], v[14:17]
	v_mfma_f32_16x16x32_bf16 v[10:13], v[94:97], v[250:253], v[10:13]
	s_setprio 0
	s_setprio 1
	v_mfma_f32_16x16x32_bf16 v[54:57], v[174:177], v[222:225], v[54:57]
	v_mfma_f32_16x16x32_bf16 v[50:53], v[214:217], v[222:225], v[50:53]
	v_mfma_f32_16x16x32_bf16 v[38:41], v[174:177], v[230:233], v[38:41]
	v_mfma_f32_16x16x32_bf16 v[34:37], v[214:217], v[230:233], v[34:37]
	v_mfma_f32_16x16x32_bf16 v[22:25], v[174:177], v[238:241], v[22:25]
	v_mfma_f32_16x16x32_bf16 v[18:21], v[214:217], v[238:241], v[18:21]
	v_mfma_f32_16x16x32_bf16 v[6:9], v[174:177], v[246:249], v[6:9]
	v_mfma_f32_16x16x32_bf16 v[2:5], v[214:217], v[246:249], v[2:5]
	v_mfma_f32_16x16x32_bf16 v[54:57], v[178:181], v[226:229], v[54:57]
	v_mfma_f32_16x16x32_bf16 v[50:53], v[218:221], v[226:229], v[50:53]
	v_mfma_f32_16x16x32_bf16 v[38:41], v[178:181], v[234:237], v[38:41]
	v_mfma_f32_16x16x32_bf16 v[34:37], v[218:221], v[234:237], v[34:37]
	v_mfma_f32_16x16x32_bf16 v[22:25], v[178:181], v[242:245], v[22:25]
	v_mfma_f32_16x16x32_bf16 v[18:21], v[218:221], v[242:245], v[18:21]
	v_mfma_f32_16x16x32_bf16 v[6:9], v[178:181], v[250:253], v[6:9]
	v_mfma_f32_16x16x32_bf16 v[2:5], v[218:221], v[250:253], v[2:5]
	s_setprio 0
	s_barrier
	s_add_i32 vcc_hi, vcc_hi, 2
	s_add_u32 s62, s62, 0x10000
	s_addc_u32 s63, s63, 0
	s_add_u32 s61, s61, 0x10000
	s_addc_u32 vcc_lo, vcc_lo, 0
	s_cmp_gt_u32 vcc_hi, 29
	s_cbranch_scc0 .LBB0_171
	s_and_b64 vcc, exec, s[48:49]
	s_cbranch_vccz .LBB0_174
	s_barrier

.LBB0_346:
	s_add_u32 s16, s56, 0x4000
	s_addc_u32 s17, s57, 0
	s_cmp_eq_u32 s70, 28
	s_cselect_b32 s62, s29, s16
	s_cselect_b32 s63, s15, s17
	s_cselect_b32 s61, s41, s69
	s_cselect_b32 s60, s49, s51
	s_add_u32 s58, s62, 0x8000
	s_addc_u32 s59, s63, 0
	s_add_i32 s16, 0, 0x10000
	v_add_u32_e32 v114, s16, v172
	s_add_i32 s17, 0, 0x14000
	ds_read_b128 v[132:135], v114
	ds_read_b128 v[136:139], v114 offset:1024
	s_waitcnt lgkmcnt(0)
	ds_read_b128 v[152:155], v114 offset:2048
	ds_read_b128 v[166:169], v114 offset:3072
	v_add_u32_e32 v114, s17, v172
	ds_read_b128 v[176:179], v114
	ds_read_b128 v[180:183], v114 offset:1024
	ds_read_b128 v[194:197], v114 offset:2048
	ds_read_b128 v[198:201], v114 offset:3072
	s_add_i32 m0, s13, 0xc000
	ds_read_b128 v[202:205], v175
	ds_read_b128 v[206:209], v175 offset:1024
	ds_read_b128 v[210:213], v175 offset:2048
	ds_read_b128 v[214:217], v175 offset:3072
	ds_read_b128 v[218:221], v175 offset:4096
	ds_read_b128 v[222:225], v175 offset:5120
	ds_read_b128 v[226:229], v175 offset:6144
	ds_read_b128 v[230:233], v175 offset:7168
	s_cmp_lg_u32 s32, 0
	s_cbranch_scc1 .Lrx_hgrn1_skip
	global_load_lds_dwordx4 v148, s[56:57]
	s_add_i32 m0, s13, 0xe000
	s_nop 0
	global_load_lds_dwordx4 v150, s[56:57]

.Lrx_hgrn1_w0:
	s_waitcnt vmcnt(24)
	s_waitcnt lgkmcnt(0)
	s_barrier
	s_setprio 1
	s_waitcnt lgkmcnt(0)
	v_mfma_f32_16x16x32_bf16 v[128:131], v[132:135], v[202:205], v[128:131]
	v_mfma_f32_16x16x32_bf16 v[124:127], v[152:155], v[202:205], v[124:127]
	v_mfma_f32_16x16x32_bf16 v[110:113], v[132:135], v[210:213], v[110:113]
	v_mfma_f32_16x16x32_bf16 v[106:109], v[152:155], v[210:213], v[106:109]
	v_mfma_f32_16x16x32_bf16 v[94:97], v[132:135], v[218:221], v[94:97]
	v_mfma_f32_16x16x32_bf16 v[90:93], v[152:155], v[218:221], v[90:93]
	v_mfma_f32_16x16x32_bf16 v[78:81], v[132:135], v[226:229], v[78:81]
	v_mfma_f32_16x16x32_bf16 v[74:77], v[152:155], v[226:229], v[74:77]
	v_mfma_f32_16x16x32_bf16 v[128:131], v[136:139], v[206:209], v[128:131]
	v_mfma_f32_16x16x32_bf16 v[124:127], v[166:169], v[206:209], v[124:127]
	v_mfma_f32_16x16x32_bf16 v[110:113], v[136:139], v[214:217], v[110:113]
	v_mfma_f32_16x16x32_bf16 v[106:109], v[166:169], v[214:217], v[106:109]
	v_mfma_f32_16x16x32_bf16 v[94:97], v[136:139], v[222:225], v[94:97]
	v_mfma_f32_16x16x32_bf16 v[90:93], v[166:169], v[222:225], v[90:93]
	v_mfma_f32_16x16x32_bf16 v[78:81], v[136:139], v[230:233], v[78:81]
	v_mfma_f32_16x16x32_bf16 v[74:77], v[166:169], v[230:233], v[74:77]
	s_setprio 0
	s_setprio 1
	v_mfma_f32_16x16x32_bf16 v[120:123], v[176:179], v[202:205], v[120:123]
	v_mfma_f32_16x16x32_bf16 v[116:119], v[194:197], v[202:205], v[116:119]
	v_mfma_f32_16x16x32_bf16 v[102:105], v[176:179], v[210:213], v[102:105]
	v_mfma_f32_16x16x32_bf16 v[98:101], v[194:197], v[210:213], v[98:101]
	v_mfma_f32_16x16x32_bf16 v[86:89], v[176:179], v[218:221], v[86:89]
	v_mfma_f32_16x16x32_bf16 v[82:85], v[194:197], v[218:221], v[82:85]
	v_mfma_f32_16x16x32_bf16 v[70:73], v[176:179], v[226:229], v[70:73]
	v_mfma_f32_16x16x32_bf16 v[66:69], v[194:197], v[226:229], v[66:69]
	v_mfma_f32_16x16x32_bf16 v[120:123], v[180:183], v[206:209], v[120:123]
	v_mfma_f32_16x16x32_bf16 v[116:119], v[198:201], v[206:209], v[116:119]
	v_mfma_f32_16x16x32_bf16 v[102:105], v[180:183], v[214:217], v[102:105]
	v_mfma_f32_16x16x32_bf16 v[98:101], v[198:201], v[214:217], v[98:101]
	v_mfma_f32_16x16x32_bf16 v[86:89], v[180:183], v[222:225], v[86:89]
	v_mfma_f32_16x16x32_bf16 v[82:85], v[198:201], v[222:225], v[82:85]
	v_mfma_f32_16x16x32_bf16 v[70:73], v[180:183], v[230:233], v[70:73]
	v_mfma_f32_16x16x32_bf16 v[66:69], v[198:201], v[230:233], v[66:69]
	s_setprio 0
	s_barrier
	s_add_i32 s16, s16, s4
	s_mov_b32 m0, s16
	ds_read_b128 v[202:205], v175 offset:16384
	ds_read_b128 v[206:209], v175 offset:17408
	ds_read_b128 v[210:213], v175 offset:18432
	ds_read_b128 v[214:217], v175 offset:19456
	ds_read_b128 v[218:221], v175 offset:20480
	ds_read_b128 v[222:225], v175 offset:21504
	ds_read_b128 v[226:229], v175 offset:22528
	ds_read_b128 v[230:233], v175 offset:23552
	global_load_lds_dwordx4 v142, s[60:61]
	s_add_i32 m0, s16, 0x2000
	s_add_u32 s74, s60, 0x1000
	s_addc_u32 s75, s61, 0
	s_add_i32 s16, s17, s4
	global_load_lds_dwordx4 v146, s[60:61]
	s_mov_b32 m0, s16
	s_nop 0
	global_load_lds_dwordx4 v142, s[74:75]
	s_add_i32 m0, s16, 0x2000
	s_nop 0
	global_load_lds_dwordx4 v146, s[74:75]
	s_mov_b32 m0, s13
	s_nop 0
	global_load_lds_dwordx4 v140, s[62:63]
	s_mov_b32 m0, s20
	s_nop 0
	global_load_lds_dwordx4 v144, s[62:63]
	s_cmp_lg_u32 s32, 0
	s_cbranch_scc1 .Lrx_hgrn1_w1
	s_waitcnt vmcnt(8)
.Lrx_hgrn1_w1:
	s_waitcnt vmcnt(24)
	s_waitcnt lgkmcnt(0)
	s_barrier
	s_setprio 1
	s_waitcnt lgkmcnt(0)
	v_mfma_f32_16x16x32_bf16 v[62:65], v[132:135], v[202:205], v[62:65]
	v_mfma_f32_16x16x32_bf16 v[58:61], v[152:155], v[202:205], v[58:61]
	v_mfma_f32_16x16x32_bf16 v[46:49], v[132:135], v[210:213], v[46:49]
	v_mfma_f32_16x16x32_bf16 v[42:45], v[152:155], v[210:213], v[42:45]
	v_mfma_f32_16x16x32_bf16 v[30:33], v[132:135], v[218:221], v[30:33]
	v_mfma_f32_16x16x32_bf16 v[26:29], v[152:155], v[218:221], v[26:29]
	v_mfma_f32_16x16x32_bf16 v[14:17], v[132:135], v[226:229], v[14:17]
	v_mfma_f32_16x16x32_bf16 v[10:13], v[152:155], v[226:229], v[10:13]
	v_mfma_f32_16x16x32_bf16 v[62:65], v[136:139], v[206:209], v[62:65]
	v_mfma_f32_16x16x32_bf16 v[58:61], v[166:169], v[206:209], v[58:61]
	v_mfma_f32_16x16x32_bf16 v[46:49], v[136:139], v[214:217], v[46:49]
	v_mfma_f32_16x16x32_bf16 v[42:45], v[166:169], v[214:217], v[42:45]
	v_mfma_f32_16x16x32_bf16 v[30:33], v[136:139], v[222:225], v[30:33]
	v_mfma_f32_16x16x32_bf16 v[26:29], v[166:169], v[222:225], v[26:29]
	v_mfma_f32_16x16x32_bf16 v[14:17], v[136:139], v[230:233], v[14:17]
	v_mfma_f32_16x16x32_bf16 v[10:13], v[166:169], v[230:233], v[10:13]
	s_setprio 0
	s_setprio 1
	v_mfma_f32_16x16x32_bf16 v[54:57], v[176:179], v[202:205], v[54:57]
	v_mfma_f32_16x16x32_bf16 v[50:53], v[194:197], v[202:205], v[50:53]
	v_mfma_f32_16x16x32_bf16 v[38:41], v[176:179], v[210:213], v[38:41]
	v_mfma_f32_16x16x32_bf16 v[34:37], v[194:197], v[210:213], v[34:37]
	v_mfma_f32_16x16x32_bf16 v[22:25], v[176:179], v[218:221], v[22:25]
	v_mfma_f32_16x16x32_bf16 v[18:21], v[194:197], v[218:221], v[18:21]
	v_mfma_f32_16x16x32_bf16 v[6:9], v[176:179], v[226:229], v[6:9]
	v_mfma_f32_16x16x32_bf16 v[2:5], v[194:197], v[226:229], v[2:5]
	v_mfma_f32_16x16x32_bf16 v[54:57], v[180:183], v[206:209], v[54:57]
	v_mfma_f32_16x16x32_bf16 v[50:53], v[198:201], v[206:209], v[50:53]
	v_mfma_f32_16x16x32_bf16 v[38:41], v[180:183], v[214:217], v[38:41]
	v_mfma_f32_16x16x32_bf16 v[34:37], v[198:201], v[214:217], v[34:37]
	v_mfma_f32_16x16x32_bf16 v[22:25], v[180:183], v[222:225], v[22:25]
	v_mfma_f32_16x16x32_bf16 v[18:21], v[198:201], v[222:225], v[18:21]
	v_mfma_f32_16x16x32_bf16 v[6:9], v[180:183], v[230:233], v[6:9]
	v_mfma_f32_16x16x32_bf16 v[2:5], v[198:201], v[230:233], v[2:5]
	s_setprio 0
	s_barrier
	s_add_i32 s16, 0, 0x18000
	v_add_u32_e32 v114, s16, v172
	s_add_i32 s17, 0, 0x1c000
	ds_read_b128 v[132:135], v114
	ds_read_b128 v[136:139], v114 offset:1024
	ds_read_b128 v[152:155], v114 offset:2048
	ds_read_b128 v[166:169], v114 offset:3072
	v_add_u32_e32 v114, s17, v172
	ds_read_b128 v[176:179], v114
	ds_read_b128 v[180:183], v114 offset:1024
	ds_read_b128 v[194:197], v114 offset:2048
	ds_read_b128 v[198:201], v114 offset:3072
	s_add_u32 s62, s62, 0x4000
	s_addc_u32 s63, s63, 0
	s_mov_b32 m0, s21
	ds_read_b128 v[202:205], v175 offset:32768
	ds_read_b128 v[206:209], v175 offset:33792
	ds_read_b128 v[210:213], v175 offset:34816
	ds_read_b128 v[214:217], v175 offset:35840
	ds_read_b128 v[218:221], v175 offset:36864
	ds_read_b128 v[222:225], v175 offset:37888
	ds_read_b128 v[226:229], v175 offset:38912
	ds_read_b128 v[230:233], v175 offset:39936
	global_load_lds_dwordx4 v140, s[62:63]
	s_mov_b32 m0, s24
	s_nop 0
	global_load_lds_dwordx4 v144, s[62:63]
	s_cmp_lg_u32 s32, 0
	s_cbranch_scc1 .Lrx_hgrn1_w2
	s_waitcnt vmcnt(8)
.Lrx_hgrn1_w2:
	s_waitcnt vmcnt(24)
	s_mov_b32 s32, 0
	s_waitcnt lgkmcnt(0)
	s_barrier
	s_setprio 1
	s_waitcnt lgkmcnt(0)
	v_mfma_f32_16x16x32_bf16 v[128:131], v[132:135], v[202:205], v[128:131]
	v_mfma_f32_16x16x32_bf16 v[124:127], v[152:155], v[202:205], v[124:127]
	v_mfma_f32_16x16x32_bf16 v[110:113], v[132:135], v[210:213], v[110:113]
	v_mfma_f32_16x16x32_bf16 v[106:109], v[152:155], v[210:213], v[106:109]
	v_mfma_f32_16x16x32_bf16 v[94:97], v[132:135], v[218:221], v[94:97]
	v_mfma_f32_16x16x32_bf16 v[90:93], v[152:155], v[218:221], v[90:93]
	v_mfma_f32_16x16x32_bf16 v[78:81], v[132:135], v[226:229], v[78:81]
	v_mfma_f32_16x16x32_bf16 v[74:77], v[152:155], v[226:229], v[74:77]
	v_mfma_f32_16x16x32_bf16 v[128:131], v[136:139], v[206:209], v[128:131]
	v_mfma_f32_16x16x32_bf16 v[124:127], v[166:169], v[206:209], v[124:127]
	v_mfma_f32_16x16x32_bf16 v[110:113], v[136:139], v[214:217], v[110:113]
	v_mfma_f32_16x16x32_bf16 v[106:109], v[166:169], v[214:217], v[106:109]
	v_mfma_f32_16x16x32_bf16 v[94:97], v[136:139], v[222:225], v[94:97]
	v_mfma_f32_16x16x32_bf16 v[90:93], v[166:169], v[222:225], v[90:93]
	v_mfma_f32_16x16x32_bf16 v[78:81], v[136:139], v[230:233], v[78:81]
	v_mfma_f32_16x16x32_bf16 v[74:77], v[166:169], v[230:233], v[74:77]
	s_setprio 0
	s_setprio 1
	v_mfma_f32_16x16x32_bf16 v[120:123], v[176:179], v[202:205], v[120:123]
	v_mfma_f32_16x16x32_bf16 v[116:119], v[194:197], v[202:205], v[116:119]
	v_mfma_f32_16x16x32_bf16 v[102:105], v[176:179], v[210:213], v[102:105]
	v_mfma_f32_16x16x32_bf16 v[98:101], v[194:197], v[210:213], v[98:101]
	v_mfma_f32_16x16x32_bf16 v[86:89], v[176:179], v[218:221], v[86:89]
	v_mfma_f32_16x16x32_bf16 v[82:85], v[194:197], v[218:221], v[82:85]
	v_mfma_f32_16x16x32_bf16 v[70:73], v[176:179], v[226:229], v[70:73]
	v_mfma_f32_16x16x32_bf16 v[66:69], v[194:197], v[226:229], v[66:69]
	v_mfma_f32_16x16x32_bf16 v[120:123], v[180:183], v[206:209], v[120:123]
	v_mfma_f32_16x16x32_bf16 v[116:119], v[198:201], v[206:209], v[116:119]
	v_mfma_f32_16x16x32_bf16 v[102:105], v[180:183], v[214:217], v[102:105]
	v_mfma_f32_16x16x32_bf16 v[98:101], v[198:201], v[214:217], v[98:101]
	v_mfma_f32_16x16x32_bf16 v[86:89], v[180:183], v[222:225], v[86:89]
	v_mfma_f32_16x16x32_bf16 v[82:85], v[198:201], v[222:225], v[82:85]
	v_mfma_f32_16x16x32_bf16 v[70:73], v[180:183], v[230:233], v[70:73]
	v_mfma_f32_16x16x32_bf16 v[66:69], v[198:201], v[230:233], v[66:69]
	s_setprio 0
	s_barrier
	s_add_u32 s62, s60, 0x8000
	s_addc_u32 s63, s61, 0
	s_add_i32 s16, s16, s4
	s_mov_b32 m0, s16
	ds_read_b128 v[202:205], v175 offset:49152
	ds_read_b128 v[206:209], v175 offset:50176
	ds_read_b128 v[210:213], v175 offset:51200
	ds_read_b128 v[214:217], v175 offset:52224
	ds_read_b128 v[218:221], v175 offset:53248
	ds_read_b128 v[222:225], v175 offset:54272
	ds_read_b128 v[226:229], v175 offset:55296
	ds_read_b128 v[230:233], v175 offset:56320
	global_load_lds_dwordx4 v142, s[62:63]
	s_add_i32 m0, s16, 0x2000
	s_add_u32 s60, s60, 0x9000
	s_addc_u32 s61, s61, 0
	s_add_i32 s16, s17, s4
	global_load_lds_dwordx4 v146, s[62:63]
	s_mov_b32 m0, s16
	s_nop 0
	global_load_lds_dwordx4 v142, s[60:61]
	s_add_i32 m0, s16, 0x2000
	s_nop 0
	global_load_lds_dwordx4 v146, s[60:61]
	s_mov_b32 m0, s65
	s_nop 0
	global_load_lds_dwordx4 v140, s[58:59]
	s_mov_b32 m0, s66
	s_nop 0
	global_load_lds_dwordx4 v144, s[58:59]
	s_waitcnt vmcnt(8)
	s_waitcnt lgkmcnt(0)
	s_barrier
	s_setprio 1
	s_waitcnt lgkmcnt(0)
	v_mfma_f32_16x16x32_bf16 v[62:65], v[132:135], v[202:205], v[62:65]
	v_mfma_f32_16x16x32_bf16 v[58:61], v[152:155], v[202:205], v[58:61]
	v_mfma_f32_16x16x32_bf16 v[46:49], v[132:135], v[210:213], v[46:49]
	v_mfma_f32_16x16x32_bf16 v[42:45], v[152:155], v[210:213], v[42:45]
	v_mfma_f32_16x16x32_bf16 v[30:33], v[132:135], v[218:221], v[30:33]
	v_mfma_f32_16x16x32_bf16 v[26:29], v[152:155], v[218:221], v[26:29]
	v_mfma_f32_16x16x32_bf16 v[14:17], v[132:135], v[226:229], v[14:17]
	v_mfma_f32_16x16x32_bf16 v[10:13], v[152:155], v[226:229], v[10:13]
	v_mfma_f32_16x16x32_bf16 v[62:65], v[136:139], v[206:209], v[62:65]
	v_mfma_f32_16x16x32_bf16 v[58:61], v[166:169], v[206:209], v[58:61]
	v_mfma_f32_16x16x32_bf16 v[46:49], v[136:139], v[214:217], v[46:49]
	v_mfma_f32_16x16x32_bf16 v[42:45], v[166:169], v[214:217], v[42:45]
	v_mfma_f32_16x16x32_bf16 v[30:33], v[136:139], v[222:225], v[30:33]
	v_mfma_f32_16x16x32_bf16 v[26:29], v[166:169], v[222:225], v[26:29]
	v_mfma_f32_16x16x32_bf16 v[14:17], v[136:139], v[230:233], v[14:17]
	v_mfma_f32_16x16x32_bf16 v[10:13], v[166:169], v[230:233], v[10:13]
	s_setprio 0
	s_setprio 1
	v_mfma_f32_16x16x32_bf16 v[54:57], v[176:179], v[202:205], v[54:57]
	v_mfma_f32_16x16x32_bf16 v[50:53], v[194:197], v[202:205], v[50:53]
	v_mfma_f32_16x16x32_bf16 v[38:41], v[176:179], v[210:213], v[38:41]
	v_mfma_f32_16x16x32_bf16 v[34:37], v[194:197], v[210:213], v[34:37]
	v_mfma_f32_16x16x32_bf16 v[22:25], v[176:179], v[218:221], v[22:25]
	v_mfma_f32_16x16x32_bf16 v[18:21], v[194:197], v[218:221], v[18:21]
	v_mfma_f32_16x16x32_bf16 v[6:9], v[176:179], v[226:229], v[6:9]
	v_mfma_f32_16x16x32_bf16 v[2:5], v[194:197], v[226:229], v[2:5]
	v_mfma_f32_16x16x32_bf16 v[54:57], v[180:183], v[206:209], v[54:57]
	v_mfma_f32_16x16x32_bf16 v[50:53], v[198:201], v[206:209], v[50:53]
	v_mfma_f32_16x16x32_bf16 v[38:41], v[180:183], v[214:217], v[38:41]
	v_mfma_f32_16x16x32_bf16 v[34:37], v[198:201], v[214:217], v[34:37]
	v_mfma_f32_16x16x32_bf16 v[22:25], v[180:183], v[222:225], v[22:25]
	v_mfma_f32_16x16x32_bf16 v[18:21], v[198:201], v[222:225], v[18:21]
	v_mfma_f32_16x16x32_bf16 v[6:9], v[180:183], v[230:233], v[6:9]
	v_mfma_f32_16x16x32_bf16 v[2:5], v[198:201], v[230:233], v[2:5]
	s_setprio 0
	s_barrier
	s_add_i32 s70, s70, 2
	s_add_u32 s56, s56, 0x10000
	s_addc_u32 s57, s57, 0
	s_add_u32 s51, s51, 0x10000
	s_addc_u32 s69, s69, 0
	s_cmp_gt_u32 s70, 29
	s_cbranch_scc0 .LBB0_346
	s_add_u32 s100, s29, 0xc000
	s_addc_u32 s101, s15, 0
	v_lshl_add_u64 v[158:159], s[100:101], 0, v[148:149]
	s_add_i32 m0, s13, 0xc000
	s_nop 0
	global_load_lds_dwordx4 v[158:159], off
	v_lshl_add_u64 v[158:159], s[100:101], 0, v[150:151]
	s_add_i32 m0, s13, 0xe000
	s_nop 0
	global_load_lds_dwordx4 v[158:159], off
	s_and_b64 vcc, exec, s[46:47]
	s_cbranch_vccz .LBB0_349
	s_barrier

.LBB0_503:
	s_add_u32 s16, s54, 0x4000
	s_addc_u32 s17, s55, 0
	s_cmp_eq_u32 s67, 28
	s_cselect_b32 s60, s29, s16
	s_cselect_b32 s61, s15, s17
	s_cselect_b32 s59, s41, s66
	s_cselect_b32 s58, s47, s49
	s_add_u32 s56, s60, 0x8000
	s_addc_u32 s57, s61, 0
	s_add_i32 s16, 0, 0x10000
	v_add_u32_e32 v114, s16, v172
	s_add_i32 s17, 0, 0x14000
	ds_read_b128 v[132:135], v114
	ds_read_b128 v[136:139], v114 offset:1024
	s_waitcnt lgkmcnt(0)
	ds_read_b128 v[152:155], v114 offset:2048
	ds_read_b128 v[166:169], v114 offset:3072
	v_add_u32_e32 v114, s17, v172
	ds_read_b128 v[176:179], v114
	ds_read_b128 v[180:183], v114 offset:1024
	ds_read_b128 v[194:197], v114 offset:2048
	ds_read_b128 v[198:201], v114 offset:3072
	s_add_i32 m0, s12, 0xc000
	ds_read_b128 v[202:205], v175
	ds_read_b128 v[206:209], v175 offset:1024
	ds_read_b128 v[210:213], v175 offset:2048
	ds_read_b128 v[214:217], v175 offset:3072
	ds_read_b128 v[218:221], v175 offset:4096
	ds_read_b128 v[222:225], v175 offset:5120
	ds_read_b128 v[226:229], v175 offset:6144
	ds_read_b128 v[230:233], v175 offset:7168
	s_cmp_lg_u32 s32, 0
	s_cbranch_scc1 .Lrx_hgrn2_skip
	global_load_lds_dwordx4 v148, s[54:55]
	s_add_i32 m0, s12, 0xe000
	s_nop 0
	global_load_lds_dwordx4 v150, s[54:55]

.Lrx_hgrn2_w0:
	s_waitcnt vmcnt(24)
	s_waitcnt lgkmcnt(0)
	s_barrier
	s_setprio 1
	s_waitcnt lgkmcnt(0)
	v_mfma_f32_16x16x32_bf16 v[128:131], v[132:135], v[202:205], v[128:131]
	v_mfma_f32_16x16x32_bf16 v[124:127], v[152:155], v[202:205], v[124:127]
	v_mfma_f32_16x16x32_bf16 v[110:113], v[132:135], v[210:213], v[110:113]
	v_mfma_f32_16x16x32_bf16 v[106:109], v[152:155], v[210:213], v[106:109]
	v_mfma_f32_16x16x32_bf16 v[94:97], v[132:135], v[218:221], v[94:97]
	v_mfma_f32_16x16x32_bf16 v[90:93], v[152:155], v[218:221], v[90:93]
	v_mfma_f32_16x16x32_bf16 v[78:81], v[132:135], v[226:229], v[78:81]
	v_mfma_f32_16x16x32_bf16 v[74:77], v[152:155], v[226:229], v[74:77]
	v_mfma_f32_16x16x32_bf16 v[128:131], v[136:139], v[206:209], v[128:131]
	v_mfma_f32_16x16x32_bf16 v[124:127], v[166:169], v[206:209], v[124:127]
	v_mfma_f32_16x16x32_bf16 v[110:113], v[136:139], v[214:217], v[110:113]
	v_mfma_f32_16x16x32_bf16 v[106:109], v[166:169], v[214:217], v[106:109]
	v_mfma_f32_16x16x32_bf16 v[94:97], v[136:139], v[222:225], v[94:97]
	v_mfma_f32_16x16x32_bf16 v[90:93], v[166:169], v[222:225], v[90:93]
	v_mfma_f32_16x16x32_bf16 v[78:81], v[136:139], v[230:233], v[78:81]
	v_mfma_f32_16x16x32_bf16 v[74:77], v[166:169], v[230:233], v[74:77]
	s_setprio 0
	s_setprio 1
	v_mfma_f32_16x16x32_bf16 v[120:123], v[176:179], v[202:205], v[120:123]
	v_mfma_f32_16x16x32_bf16 v[116:119], v[194:197], v[202:205], v[116:119]
	v_mfma_f32_16x16x32_bf16 v[102:105], v[176:179], v[210:213], v[102:105]
	v_mfma_f32_16x16x32_bf16 v[98:101], v[194:197], v[210:213], v[98:101]
	v_mfma_f32_16x16x32_bf16 v[86:89], v[176:179], v[218:221], v[86:89]
	v_mfma_f32_16x16x32_bf16 v[82:85], v[194:197], v[218:221], v[82:85]
	v_mfma_f32_16x16x32_bf16 v[70:73], v[176:179], v[226:229], v[70:73]
	v_mfma_f32_16x16x32_bf16 v[66:69], v[194:197], v[226:229], v[66:69]
	v_mfma_f32_16x16x32_bf16 v[120:123], v[180:183], v[206:209], v[120:123]
	v_mfma_f32_16x16x32_bf16 v[116:119], v[198:201], v[206:209], v[116:119]
	v_mfma_f32_16x16x32_bf16 v[102:105], v[180:183], v[214:217], v[102:105]
	v_mfma_f32_16x16x32_bf16 v[98:101], v[198:201], v[214:217], v[98:101]
	v_mfma_f32_16x16x32_bf16 v[86:89], v[180:183], v[222:225], v[86:89]
	v_mfma_f32_16x16x32_bf16 v[82:85], v[198:201], v[222:225], v[82:85]
	v_mfma_f32_16x16x32_bf16 v[70:73], v[180:183], v[230:233], v[70:73]
	v_mfma_f32_16x16x32_bf16 v[66:69], v[198:201], v[230:233], v[66:69]
	s_setprio 0
	s_barrier
	s_add_i32 s16, s16, s4
	s_mov_b32 m0, s16
	ds_read_b128 v[202:205], v175 offset:16384
	ds_read_b128 v[206:209], v175 offset:17408
	ds_read_b128 v[210:213], v175 offset:18432
	ds_read_b128 v[214:217], v175 offset:19456
	ds_read_b128 v[218:221], v175 offset:20480
	ds_read_b128 v[222:225], v175 offset:21504
	ds_read_b128 v[226:229], v175 offset:22528
	ds_read_b128 v[230:233], v175 offset:23552
	global_load_lds_dwordx4 v142, s[58:59]
	s_add_i32 m0, s16, 0x2000
	s_add_u32 s68, s58, 0x1000
	s_addc_u32 s69, s59, 0
	s_add_i32 s16, s17, s4
	global_load_lds_dwordx4 v146, s[58:59]
	s_mov_b32 m0, s16
	s_nop 0
	global_load_lds_dwordx4 v142, s[68:69]
	s_add_i32 m0, s16, 0x2000
	s_nop 0
	global_load_lds_dwordx4 v146, s[68:69]
	s_mov_b32 m0, s12
	s_nop 0
	global_load_lds_dwordx4 v140, s[60:61]
	s_mov_b32 m0, s13
	s_nop 0
	global_load_lds_dwordx4 v144, s[60:61]
	s_cmp_lg_u32 s32, 0
	s_cbranch_scc1 .Lrx_hgrn2_w1
	s_waitcnt vmcnt(8)
.Lrx_hgrn2_w1:
	s_waitcnt vmcnt(24)
	s_waitcnt lgkmcnt(0)
	s_barrier
	s_setprio 1
	s_waitcnt lgkmcnt(0)
	v_mfma_f32_16x16x32_bf16 v[62:65], v[132:135], v[202:205], v[62:65]
	v_mfma_f32_16x16x32_bf16 v[58:61], v[152:155], v[202:205], v[58:61]
	v_mfma_f32_16x16x32_bf16 v[46:49], v[132:135], v[210:213], v[46:49]
	v_mfma_f32_16x16x32_bf16 v[42:45], v[152:155], v[210:213], v[42:45]
	v_mfma_f32_16x16x32_bf16 v[30:33], v[132:135], v[218:221], v[30:33]
	v_mfma_f32_16x16x32_bf16 v[26:29], v[152:155], v[218:221], v[26:29]
	v_mfma_f32_16x16x32_bf16 v[14:17], v[132:135], v[226:229], v[14:17]
	v_mfma_f32_16x16x32_bf16 v[10:13], v[152:155], v[226:229], v[10:13]
	v_mfma_f32_16x16x32_bf16 v[62:65], v[136:139], v[206:209], v[62:65]
	v_mfma_f32_16x16x32_bf16 v[58:61], v[166:169], v[206:209], v[58:61]
	v_mfma_f32_16x16x32_bf16 v[46:49], v[136:139], v[214:217], v[46:49]
	v_mfma_f32_16x16x32_bf16 v[42:45], v[166:169], v[214:217], v[42:45]
	v_mfma_f32_16x16x32_bf16 v[30:33], v[136:139], v[222:225], v[30:33]
	v_mfma_f32_16x16x32_bf16 v[26:29], v[166:169], v[222:225], v[26:29]
	v_mfma_f32_16x16x32_bf16 v[14:17], v[136:139], v[230:233], v[14:17]
	v_mfma_f32_16x16x32_bf16 v[10:13], v[166:169], v[230:233], v[10:13]
	s_setprio 0
	s_setprio 1
	v_mfma_f32_16x16x32_bf16 v[54:57], v[176:179], v[202:205], v[54:57]
	v_mfma_f32_16x16x32_bf16 v[50:53], v[194:197], v[202:205], v[50:53]
	v_mfma_f32_16x16x32_bf16 v[38:41], v[176:179], v[210:213], v[38:41]
	v_mfma_f32_16x16x32_bf16 v[34:37], v[194:197], v[210:213], v[34:37]
	v_mfma_f32_16x16x32_bf16 v[22:25], v[176:179], v[218:221], v[22:25]
	v_mfma_f32_16x16x32_bf16 v[18:21], v[194:197], v[218:221], v[18:21]
	v_mfma_f32_16x16x32_bf16 v[6:9], v[176:179], v[226:229], v[6:9]
	v_mfma_f32_16x16x32_bf16 v[2:5], v[194:197], v[226:229], v[2:5]
	v_mfma_f32_16x16x32_bf16 v[54:57], v[180:183], v[206:209], v[54:57]
	v_mfma_f32_16x16x32_bf16 v[50:53], v[198:201], v[206:209], v[50:53]
	v_mfma_f32_16x16x32_bf16 v[38:41], v[180:183], v[214:217], v[38:41]
	v_mfma_f32_16x16x32_bf16 v[34:37], v[198:201], v[214:217], v[34:37]
	v_mfma_f32_16x16x32_bf16 v[22:25], v[180:183], v[222:225], v[22:25]
	v_mfma_f32_16x16x32_bf16 v[18:21], v[198:201], v[222:225], v[18:21]
	v_mfma_f32_16x16x32_bf16 v[6:9], v[180:183], v[230:233], v[6:9]
	v_mfma_f32_16x16x32_bf16 v[2:5], v[198:201], v[230:233], v[2:5]
	s_setprio 0
	s_barrier
	s_add_i32 s16, 0, 0x18000
	v_add_u32_e32 v114, s16, v172
	s_add_i32 s17, 0, 0x1c000
	ds_read_b128 v[132:135], v114
	ds_read_b128 v[136:139], v114 offset:1024
	ds_read_b128 v[152:155], v114 offset:2048
	ds_read_b128 v[166:169], v114 offset:3072
	v_add_u32_e32 v114, s17, v172
	ds_read_b128 v[176:179], v114
	ds_read_b128 v[180:183], v114 offset:1024
	ds_read_b128 v[194:197], v114 offset:2048
	ds_read_b128 v[198:201], v114 offset:3072
	s_add_u32 s60, s60, 0x4000
	s_addc_u32 s61, s61, 0
	s_mov_b32 m0, s20
	ds_read_b128 v[202:205], v175 offset:32768
	ds_read_b128 v[206:209], v175 offset:33792
	ds_read_b128 v[210:213], v175 offset:34816
	ds_read_b128 v[214:217], v175 offset:35840
	ds_read_b128 v[218:221], v175 offset:36864
	ds_read_b128 v[222:225], v175 offset:37888
	ds_read_b128 v[226:229], v175 offset:38912
	ds_read_b128 v[230:233], v175 offset:39936
	global_load_lds_dwordx4 v140, s[60:61]
	s_mov_b32 m0, s21
	s_nop 0
	global_load_lds_dwordx4 v144, s[60:61]
	s_cmp_lg_u32 s32, 0
	s_cbranch_scc1 .Lrx_hgrn2_w2
	s_waitcnt vmcnt(8)
.Lrx_hgrn2_w2:
	s_waitcnt vmcnt(24)
	s_mov_b32 s32, 0
	s_waitcnt lgkmcnt(0)
	s_barrier
	s_setprio 1
	s_waitcnt lgkmcnt(0)
	v_mfma_f32_16x16x32_bf16 v[128:131], v[132:135], v[202:205], v[128:131]
	v_mfma_f32_16x16x32_bf16 v[124:127], v[152:155], v[202:205], v[124:127]
	v_mfma_f32_16x16x32_bf16 v[110:113], v[132:135], v[210:213], v[110:113]
	v_mfma_f32_16x16x32_bf16 v[106:109], v[152:155], v[210:213], v[106:109]
	v_mfma_f32_16x16x32_bf16 v[94:97], v[132:135], v[218:221], v[94:97]
	v_mfma_f32_16x16x32_bf16 v[90:93], v[152:155], v[218:221], v[90:93]
	v_mfma_f32_16x16x32_bf16 v[78:81], v[132:135], v[226:229], v[78:81]
	v_mfma_f32_16x16x32_bf16 v[74:77], v[152:155], v[226:229], v[74:77]
	v_mfma_f32_16x16x32_bf16 v[128:131], v[136:139], v[206:209], v[128:131]
	v_mfma_f32_16x16x32_bf16 v[124:127], v[166:169], v[206:209], v[124:127]
	v_mfma_f32_16x16x32_bf16 v[110:113], v[136:139], v[214:217], v[110:113]
	v_mfma_f32_16x16x32_bf16 v[106:109], v[166:169], v[214:217], v[106:109]
	v_mfma_f32_16x16x32_bf16 v[94:97], v[136:139], v[222:225], v[94:97]
	v_mfma_f32_16x16x32_bf16 v[90:93], v[166:169], v[222:225], v[90:93]
	v_mfma_f32_16x16x32_bf16 v[78:81], v[136:139], v[230:233], v[78:81]
	v_mfma_f32_16x16x32_bf16 v[74:77], v[166:169], v[230:233], v[74:77]
	s_setprio 0
	s_setprio 1
	v_mfma_f32_16x16x32_bf16 v[120:123], v[176:179], v[202:205], v[120:123]
	v_mfma_f32_16x16x32_bf16 v[116:119], v[194:197], v[202:205], v[116:119]
	v_mfma_f32_16x16x32_bf16 v[102:105], v[176:179], v[210:213], v[102:105]
	v_mfma_f32_16x16x32_bf16 v[98:101], v[194:197], v[210:213], v[98:101]
	v_mfma_f32_16x16x32_bf16 v[86:89], v[176:179], v[218:221], v[86:89]
	v_mfma_f32_16x16x32_bf16 v[82:85], v[194:197], v[218:221], v[82:85]
	v_mfma_f32_16x16x32_bf16 v[70:73], v[176:179], v[226:229], v[70:73]
	v_mfma_f32_16x16x32_bf16 v[66:69], v[194:197], v[226:229], v[66:69]
	v_mfma_f32_16x16x32_bf16 v[120:123], v[180:183], v[206:209], v[120:123]
	v_mfma_f32_16x16x32_bf16 v[116:119], v[198:201], v[206:209], v[116:119]
	v_mfma_f32_16x16x32_bf16 v[102:105], v[180:183], v[214:217], v[102:105]
	v_mfma_f32_16x16x32_bf16 v[98:101], v[198:201], v[214:217], v[98:101]
	v_mfma_f32_16x16x32_bf16 v[86:89], v[180:183], v[222:225], v[86:89]
	v_mfma_f32_16x16x32_bf16 v[82:85], v[198:201], v[222:225], v[82:85]
	v_mfma_f32_16x16x32_bf16 v[70:73], v[180:183], v[230:233], v[70:73]
	v_mfma_f32_16x16x32_bf16 v[66:69], v[198:201], v[230:233], v[66:69]
	s_setprio 0
	s_barrier
	s_add_u32 s60, s58, 0x8000
	s_addc_u32 s61, s59, 0
	s_add_i32 s16, s16, s4
	s_mov_b32 m0, s16
	ds_read_b128 v[202:205], v175 offset:49152
	ds_read_b128 v[206:209], v175 offset:50176
	ds_read_b128 v[210:213], v175 offset:51200
	ds_read_b128 v[214:217], v175 offset:52224
	ds_read_b128 v[218:221], v175 offset:53248
	ds_read_b128 v[222:225], v175 offset:54272
	ds_read_b128 v[226:229], v175 offset:55296
	ds_read_b128 v[230:233], v175 offset:56320
	global_load_lds_dwordx4 v142, s[60:61]
	s_add_i32 m0, s16, 0x2000
	s_add_u32 s58, s58, 0x9000
	s_addc_u32 s59, s59, 0
	s_add_i32 s16, s17, s4
	global_load_lds_dwordx4 v146, s[60:61]
	s_mov_b32 m0, s16
	s_nop 0
	global_load_lds_dwordx4 v142, s[58:59]
	s_add_i32 m0, s16, 0x2000
	s_nop 0
	global_load_lds_dwordx4 v146, s[58:59]
	s_mov_b32 m0, s62
	s_nop 0
	global_load_lds_dwordx4 v140, s[56:57]
	s_mov_b32 m0, s63
	s_nop 0
	global_load_lds_dwordx4 v144, s[56:57]
	s_waitcnt vmcnt(8)
	s_waitcnt lgkmcnt(0)
	s_barrier
	s_setprio 1
	s_waitcnt lgkmcnt(0)
	v_mfma_f32_16x16x32_bf16 v[62:65], v[132:135], v[202:205], v[62:65]
	v_mfma_f32_16x16x32_bf16 v[58:61], v[152:155], v[202:205], v[58:61]
	v_mfma_f32_16x16x32_bf16 v[46:49], v[132:135], v[210:213], v[46:49]
	v_mfma_f32_16x16x32_bf16 v[42:45], v[152:155], v[210:213], v[42:45]
	v_mfma_f32_16x16x32_bf16 v[30:33], v[132:135], v[218:221], v[30:33]
	v_mfma_f32_16x16x32_bf16 v[26:29], v[152:155], v[218:221], v[26:29]
	v_mfma_f32_16x16x32_bf16 v[14:17], v[132:135], v[226:229], v[14:17]
	v_mfma_f32_16x16x32_bf16 v[10:13], v[152:155], v[226:229], v[10:13]
	v_mfma_f32_16x16x32_bf16 v[62:65], v[136:139], v[206:209], v[62:65]
	v_mfma_f32_16x16x32_bf16 v[58:61], v[166:169], v[206:209], v[58:61]
	v_mfma_f32_16x16x32_bf16 v[46:49], v[136:139], v[214:217], v[46:49]
	v_mfma_f32_16x16x32_bf16 v[42:45], v[166:169], v[214:217], v[42:45]
	v_mfma_f32_16x16x32_bf16 v[30:33], v[136:139], v[222:225], v[30:33]
	v_mfma_f32_16x16x32_bf16 v[26:29], v[166:169], v[222:225], v[26:29]
	v_mfma_f32_16x16x32_bf16 v[14:17], v[136:139], v[230:233], v[14:17]
	v_mfma_f32_16x16x32_bf16 v[10:13], v[166:169], v[230:233], v[10:13]
	s_setprio 0
	s_setprio 1
	v_mfma_f32_16x16x32_bf16 v[54:57], v[176:179], v[202:205], v[54:57]
	v_mfma_f32_16x16x32_bf16 v[50:53], v[194:197], v[202:205], v[50:53]
	v_mfma_f32_16x16x32_bf16 v[38:41], v[176:179], v[210:213], v[38:41]
	v_mfma_f32_16x16x32_bf16 v[34:37], v[194:197], v[210:213], v[34:37]
	v_mfma_f32_16x16x32_bf16 v[22:25], v[176:179], v[218:221], v[22:25]
	v_mfma_f32_16x16x32_bf16 v[18:21], v[194:197], v[218:221], v[18:21]
	v_mfma_f32_16x16x32_bf16 v[6:9], v[176:179], v[226:229], v[6:9]
	v_mfma_f32_16x16x32_bf16 v[2:5], v[194:197], v[226:229], v[2:5]
	v_mfma_f32_16x16x32_bf16 v[54:57], v[180:183], v[206:209], v[54:57]
	v_mfma_f32_16x16x32_bf16 v[50:53], v[198:201], v[206:209], v[50:53]
	v_mfma_f32_16x16x32_bf16 v[38:41], v[180:183], v[214:217], v[38:41]
	v_mfma_f32_16x16x32_bf16 v[34:37], v[198:201], v[214:217], v[34:37]
	v_mfma_f32_16x16x32_bf16 v[22:25], v[180:183], v[222:225], v[22:25]
	v_mfma_f32_16x16x32_bf16 v[18:21], v[198:201], v[222:225], v[18:21]
	v_mfma_f32_16x16x32_bf16 v[6:9], v[180:183], v[230:233], v[6:9]
	v_mfma_f32_16x16x32_bf16 v[2:5], v[198:201], v[230:233], v[2:5]
	s_setprio 0
	s_barrier
	s_add_i32 s67, s67, 2
	s_add_u32 s54, s54, 0x10000
	s_addc_u32 s55, s55, 0
	s_add_u32 s49, s49, 0x10000
	s_addc_u32 s66, s66, 0
	s_cmp_gt_u32 s67, 29
	s_cbranch_scc0 .LBB0_503
	s_add_u32 s100, s29, 0xc000
	s_addc_u32 s101, s15, 0
	v_lshl_add_u64 v[158:159], s[100:101], 0, v[148:149]
	s_add_i32 m0, s12, 0xc000
	s_nop 0
	global_load_lds_dwordx4 v[158:159], off
	v_lshl_add_u64 v[158:159], s[100:101], 0, v[150:151]
	s_add_i32 m0, s12, 0xe000
	s_nop 0
	global_load_lds_dwordx4 v[158:159], off
	s_and_b64 vcc, exec, s[44:45]
	s_cbranch_vccz .LBB0_506
	s_barrier

.LBB0_1079:
	s_add_u32 s16, s52, 0x4000
	s_addc_u32 s17, s53, 0
	s_cmp_eq_u32 s64, 28
	s_cselect_b32 s56, s29, s16
	s_cselect_b32 s57, s24, s17
	s_cselect_b32 s55, s27, s63
	s_cselect_b32 s54, s47, s49
	s_add_u32 s50, s56, 0x8000
	s_addc_u32 s51, s57, 0
	s_add_i32 s16, 0, 0x10000
	v_add_u32_e32 v144, s16, v146
	s_add_i32 s65, 0, 0x14000
	ds_read_b128 v[148:151], v144
	ds_read_b128 v[152:155], v144 offset:1024
	ds_read_b128 v[158:161], v144 offset:2048
	ds_read_b128 v[166:169], v144 offset:3072
	v_add_u32_e32 v144, s65, v146
	ds_read_b128 v[170:173], v144
	ds_read_b128 v[174:177], v144 offset:1024
	ds_read_b128 v[178:181], v144 offset:2048
	ds_read_b128 v[194:197], v144 offset:3072
	s_add_i32 m0, s20, 0xc000
	ds_read_b128 v[198:201], v147
	ds_read_b128 v[202:205], v147 offset:1024
	ds_read_b128 v[206:209], v147 offset:2048
	ds_read_b128 v[210:213], v147 offset:3072
	ds_read_b128 v[214:217], v147 offset:4096
	ds_read_b128 v[218:221], v147 offset:5120
	ds_read_b128 v[222:225], v147 offset:6144
	ds_read_b128 v[226:229], v147 offset:7168
	global_load_lds_dwordx4 v140, s[52:53]
	s_add_i32 m0, s20, 0xe000
	s_nop 0
	global_load_lds_dwordx4 v142, s[52:53]
	s_waitcnt vmcnt(8)
	s_waitcnt lgkmcnt(0)
	s_barrier
	s_setprio 1
	s_waitcnt lgkmcnt(0)
	v_mfma_f32_16x16x32_bf16 v[116:119], v[148:151], v[198:201], v[116:119]
	v_mfma_f32_16x16x32_bf16 v[124:127], v[158:161], v[198:201], v[124:127]
	v_mfma_f32_16x16x32_bf16 v[98:101], v[148:151], v[206:209], v[98:101]
	v_mfma_f32_16x16x32_bf16 v[102:105], v[158:161], v[206:209], v[102:105]
	v_mfma_f32_16x16x32_bf16 v[82:85], v[148:151], v[214:217], v[82:85]
	v_mfma_f32_16x16x32_bf16 v[90:93], v[158:161], v[214:217], v[90:93]
	v_mfma_f32_16x16x32_bf16 v[58:61], v[148:151], v[222:225], v[58:61]
	v_mfma_f32_16x16x32_bf16 v[70:73], v[158:161], v[222:225], v[70:73]
	v_mfma_f32_16x16x32_bf16 v[116:119], v[152:155], v[202:205], v[116:119]
	v_mfma_f32_16x16x32_bf16 v[124:127], v[166:169], v[202:205], v[124:127]
	v_mfma_f32_16x16x32_bf16 v[98:101], v[152:155], v[210:213], v[98:101]
	v_mfma_f32_16x16x32_bf16 v[102:105], v[166:169], v[210:213], v[102:105]
	v_mfma_f32_16x16x32_bf16 v[82:85], v[152:155], v[218:221], v[82:85]
	v_mfma_f32_16x16x32_bf16 v[90:93], v[166:169], v[218:221], v[90:93]
	v_mfma_f32_16x16x32_bf16 v[58:61], v[152:155], v[226:229], v[58:61]
	v_mfma_f32_16x16x32_bf16 v[70:73], v[166:169], v[226:229], v[70:73]
	s_setprio 0
	s_setprio 1
	v_mfma_f32_16x16x32_bf16 v[120:123], v[170:173], v[198:201], v[120:123]
	v_mfma_f32_16x16x32_bf16 v[128:131], v[178:181], v[198:201], v[128:131]
	v_mfma_f32_16x16x32_bf16 v[106:109], v[170:173], v[206:209], v[106:109]
	v_mfma_f32_16x16x32_bf16 v[110:113], v[178:181], v[206:209], v[110:113]
	v_mfma_f32_16x16x32_bf16 v[86:89], v[170:173], v[214:217], v[86:89]
	v_mfma_f32_16x16x32_bf16 v[94:97], v[178:181], v[214:217], v[94:97]
	v_mfma_f32_16x16x32_bf16 v[74:77], v[170:173], v[222:225], v[74:77]
	v_mfma_f32_16x16x32_bf16 v[78:81], v[178:181], v[222:225], v[78:81]
	v_mfma_f32_16x16x32_bf16 v[120:123], v[174:177], v[202:205], v[120:123]
	v_mfma_f32_16x16x32_bf16 v[128:131], v[194:197], v[202:205], v[128:131]
	v_mfma_f32_16x16x32_bf16 v[106:109], v[174:177], v[210:213], v[106:109]
	v_mfma_f32_16x16x32_bf16 v[110:113], v[194:197], v[210:213], v[110:113]
	v_mfma_f32_16x16x32_bf16 v[86:89], v[174:177], v[218:221], v[86:89]
	v_mfma_f32_16x16x32_bf16 v[94:97], v[194:197], v[218:221], v[94:97]
	v_mfma_f32_16x16x32_bf16 v[74:77], v[174:177], v[226:229], v[74:77]
	v_mfma_f32_16x16x32_bf16 v[78:81], v[194:197], v[226:229], v[78:81]
	s_setprio 0
	s_barrier
	s_add_i32 s16, s16, s13
	s_mov_b32 m0, s16
	ds_read_b128 v[198:201], v147 offset:16384
	ds_read_b128 v[202:205], v147 offset:17408
	ds_read_b128 v[206:209], v147 offset:18432
	ds_read_b128 v[210:213], v147 offset:19456
	ds_read_b128 v[214:217], v147 offset:20480
	ds_read_b128 v[218:221], v147 offset:21504
	ds_read_b128 v[222:225], v147 offset:22528
	ds_read_b128 v[226:229], v147 offset:23552
	global_load_lds_dwordx4 v114, s[54:55]
	s_add_i32 m0, s16, 0x2000
	s_add_u32 s16, s54, 0x1000
	s_addc_u32 s17, s55, 0
	s_add_i32 s65, s65, s13
	global_load_lds_dwordx4 v136, s[54:55]
	s_mov_b32 m0, s65
	s_nop 0
	global_load_lds_dwordx4 v114, s[16:17]
	s_add_i32 m0, s65, 0x2000
	s_nop 0
	global_load_lds_dwordx4 v136, s[16:17]
	s_mov_b32 m0, s20
	s_nop 0
	global_load_lds_dwordx4 v132, s[56:57]
	s_mov_b32 m0, s21
	s_nop 0
	global_load_lds_dwordx4 v134, s[56:57]
	s_waitcnt vmcnt(8)
	s_waitcnt lgkmcnt(0)
	s_barrier
	s_setprio 1
	s_waitcnt lgkmcnt(0)
	v_mfma_f32_16x16x32_bf16 v[50:53], v[148:151], v[198:201], v[50:53]
	v_mfma_f32_16x16x32_bf16 v[62:65], v[158:161], v[198:201], v[62:65]
	v_mfma_f32_16x16x32_bf16 v[34:37], v[148:151], v[206:209], v[34:37]
	v_mfma_f32_16x16x32_bf16 v[38:41], v[158:161], v[206:209], v[38:41]
	v_mfma_f32_16x16x32_bf16 v[18:21], v[148:151], v[214:217], v[18:21]
	v_mfma_f32_16x16x32_bf16 v[26:29], v[158:161], v[214:217], v[26:29]
	v_mfma_f32_16x16x32_bf16 v[2:5], v[148:151], v[222:225], v[2:5]
	v_mfma_f32_16x16x32_bf16 v[6:9], v[158:161], v[222:225], v[6:9]
	v_mfma_f32_16x16x32_bf16 v[50:53], v[152:155], v[202:205], v[50:53]
	v_mfma_f32_16x16x32_bf16 v[62:65], v[166:169], v[202:205], v[62:65]
	v_mfma_f32_16x16x32_bf16 v[34:37], v[152:155], v[210:213], v[34:37]
	v_mfma_f32_16x16x32_bf16 v[38:41], v[166:169], v[210:213], v[38:41]
	v_mfma_f32_16x16x32_bf16 v[18:21], v[152:155], v[218:221], v[18:21]
	v_mfma_f32_16x16x32_bf16 v[26:29], v[166:169], v[218:221], v[26:29]
	v_mfma_f32_16x16x32_bf16 v[2:5], v[152:155], v[226:229], v[2:5]
	v_mfma_f32_16x16x32_bf16 v[6:9], v[166:169], v[226:229], v[6:9]
	s_setprio 0
	s_setprio 1
	v_mfma_f32_16x16x32_bf16 v[54:57], v[170:173], v[198:201], v[54:57]
	v_mfma_f32_16x16x32_bf16 v[66:69], v[178:181], v[198:201], v[66:69]
	v_mfma_f32_16x16x32_bf16 v[42:45], v[170:173], v[206:209], v[42:45]
	v_mfma_f32_16x16x32_bf16 v[46:49], v[178:181], v[206:209], v[46:49]
	v_mfma_f32_16x16x32_bf16 v[22:25], v[170:173], v[214:217], v[22:25]
	v_mfma_f32_16x16x32_bf16 v[30:33], v[178:181], v[214:217], v[30:33]
	v_mfma_f32_16x16x32_bf16 v[10:13], v[170:173], v[222:225], v[10:13]
	v_mfma_f32_16x16x32_bf16 v[14:17], v[178:181], v[222:225], v[14:17]
	v_mfma_f32_16x16x32_bf16 v[54:57], v[174:177], v[202:205], v[54:57]
	v_mfma_f32_16x16x32_bf16 v[66:69], v[194:197], v[202:205], v[66:69]
	v_mfma_f32_16x16x32_bf16 v[42:45], v[174:177], v[210:213], v[42:45]
	v_mfma_f32_16x16x32_bf16 v[46:49], v[194:197], v[210:213], v[46:49]
	v_mfma_f32_16x16x32_bf16 v[22:25], v[174:177], v[218:221], v[22:25]
	v_mfma_f32_16x16x32_bf16 v[30:33], v[194:197], v[218:221], v[30:33]
	v_mfma_f32_16x16x32_bf16 v[10:13], v[174:177], v[226:229], v[10:13]
	v_mfma_f32_16x16x32_bf16 v[14:17], v[194:197], v[226:229], v[14:17]
	s_setprio 0
	s_barrier
	s_add_i32 s65, 0, 0x18000
	v_add_u32_e32 v144, s65, v146
	s_add_i32 s66, 0, 0x1c000
	ds_read_b128 v[148:151], v144
	ds_read_b128 v[152:155], v144 offset:1024
	ds_read_b128 v[158:161], v144 offset:2048
	ds_read_b128 v[166:169], v144 offset:3072
	v_add_u32_e32 v144, s66, v146
	ds_read_b128 v[170:173], v144
	ds_read_b128 v[174:177], v144 offset:1024
	ds_read_b128 v[178:181], v144 offset:2048
	ds_read_b128 v[194:197], v144 offset:3072
	s_add_u32 s16, s56, 0x4000
	s_addc_u32 s17, s57, 0
	s_mov_b32 m0, s37
	ds_read_b128 v[198:201], v147 offset:32768
	ds_read_b128 v[202:205], v147 offset:33792
	ds_read_b128 v[206:209], v147 offset:34816
	ds_read_b128 v[210:213], v147 offset:35840
	ds_read_b128 v[214:217], v147 offset:36864
	ds_read_b128 v[218:221], v147 offset:37888
	ds_read_b128 v[222:225], v147 offset:38912
	ds_read_b128 v[226:229], v147 offset:39936
	global_load_lds_dwordx4 v132, s[16:17]
	s_mov_b32 m0, s58
	s_nop 0
	global_load_lds_dwordx4 v134, s[16:17]
	s_waitcnt vmcnt(8)
	s_waitcnt lgkmcnt(0)
	s_barrier
	s_setprio 1
	s_waitcnt lgkmcnt(0)
	v_mfma_f32_16x16x32_bf16 v[116:119], v[148:151], v[198:201], v[116:119]
	v_mfma_f32_16x16x32_bf16 v[124:127], v[158:161], v[198:201], v[124:127]
	v_mfma_f32_16x16x32_bf16 v[98:101], v[148:151], v[206:209], v[98:101]
	v_mfma_f32_16x16x32_bf16 v[102:105], v[158:161], v[206:209], v[102:105]
	v_mfma_f32_16x16x32_bf16 v[82:85], v[148:151], v[214:217], v[82:85]
	v_mfma_f32_16x16x32_bf16 v[90:93], v[158:161], v[214:217], v[90:93]
	v_mfma_f32_16x16x32_bf16 v[58:61], v[148:151], v[222:225], v[58:61]
	v_mfma_f32_16x16x32_bf16 v[70:73], v[158:161], v[222:225], v[70:73]
	v_mfma_f32_16x16x32_bf16 v[116:119], v[152:155], v[202:205], v[116:119]
	v_mfma_f32_16x16x32_bf16 v[124:127], v[166:169], v[202:205], v[124:127]
	v_mfma_f32_16x16x32_bf16 v[98:101], v[152:155], v[210:213], v[98:101]
	v_mfma_f32_16x16x32_bf16 v[102:105], v[166:169], v[210:213], v[102:105]
	v_mfma_f32_16x16x32_bf16 v[82:85], v[152:155], v[218:221], v[82:85]
	v_mfma_f32_16x16x32_bf16 v[90:93], v[166:169], v[218:221], v[90:93]
	v_mfma_f32_16x16x32_bf16 v[58:61], v[152:155], v[226:229], v[58:61]
	v_mfma_f32_16x16x32_bf16 v[70:73], v[166:169], v[226:229], v[70:73]
	s_setprio 0
	s_setprio 1
	v_mfma_f32_16x16x32_bf16 v[120:123], v[170:173], v[198:201], v[120:123]
	v_mfma_f32_16x16x32_bf16 v[128:131], v[178:181], v[198:201], v[128:131]
	v_mfma_f32_16x16x32_bf16 v[106:109], v[170:173], v[206:209], v[106:109]
	v_mfma_f32_16x16x32_bf16 v[110:113], v[178:181], v[206:209], v[110:113]
	v_mfma_f32_16x16x32_bf16 v[86:89], v[170:173], v[214:217], v[86:89]
	v_mfma_f32_16x16x32_bf16 v[94:97], v[178:181], v[214:217], v[94:97]
	v_mfma_f32_16x16x32_bf16 v[74:77], v[170:173], v[222:225], v[74:77]
	v_mfma_f32_16x16x32_bf16 v[78:81], v[178:181], v[222:225], v[78:81]
	v_mfma_f32_16x16x32_bf16 v[120:123], v[174:177], v[202:205], v[120:123]
	v_mfma_f32_16x16x32_bf16 v[128:131], v[194:197], v[202:205], v[128:131]
	v_mfma_f32_16x16x32_bf16 v[106:109], v[174:177], v[210:213], v[106:109]
	v_mfma_f32_16x16x32_bf16 v[110:113], v[194:197], v[210:213], v[110:113]
	v_mfma_f32_16x16x32_bf16 v[86:89], v[174:177], v[218:221], v[86:89]
	v_mfma_f32_16x16x32_bf16 v[94:97], v[194:197], v[218:221], v[94:97]
	v_mfma_f32_16x16x32_bf16 v[74:77], v[174:177], v[226:229], v[74:77]
	v_mfma_f32_16x16x32_bf16 v[78:81], v[194:197], v[226:229], v[78:81]
	s_setprio 0
	s_barrier
	s_add_u32 s16, s54, 0x8000
	s_addc_u32 s17, s55, 0
	s_add_i32 s56, s65, s13
	s_mov_b32 m0, s56
	ds_read_b128 v[198:201], v147 offset:49152
	ds_read_b128 v[202:205], v147 offset:50176
	ds_read_b128 v[206:209], v147 offset:51200
	ds_read_b128 v[210:213], v147 offset:52224
	ds_read_b128 v[214:217], v147 offset:53248
	ds_read_b128 v[218:221], v147 offset:54272
	ds_read_b128 v[222:225], v147 offset:55296
	ds_read_b128 v[226:229], v147 offset:56320
	global_load_lds_dwordx4 v114, s[16:17]
	s_add_i32 m0, s56, 0x2000
	v_lshl_add_u64 v[144:145], s[16:17], 0, v[136:137]
	s_add_u32 s16, s54, 0x9000
	s_addc_u32 s17, s55, 0
	s_add_i32 s54, s66, s13
	global_load_lds_dwordx4 v[144:145], off
	s_mov_b32 m0, s54
	s_nop 0
	global_load_lds_dwordx4 v114, s[16:17]
	s_add_i32 m0, s54, 0x2000
	s_nop 0
	global_load_lds_dwordx4 v136, s[16:17]
	s_mov_b32 m0, s59
	s_nop 0
	global_load_lds_dwordx4 v132, s[50:51]
	s_mov_b32 m0, s60
	s_nop 0
	global_load_lds_dwordx4 v134, s[50:51]
	s_waitcnt vmcnt(8)
	s_waitcnt lgkmcnt(0)
	s_barrier
	s_setprio 1
	s_waitcnt lgkmcnt(0)
	v_mfma_f32_16x16x32_bf16 v[50:53], v[148:151], v[198:201], v[50:53]
	v_mfma_f32_16x16x32_bf16 v[62:65], v[158:161], v[198:201], v[62:65]
	v_mfma_f32_16x16x32_bf16 v[34:37], v[148:151], v[206:209], v[34:37]
	v_mfma_f32_16x16x32_bf16 v[38:41], v[158:161], v[206:209], v[38:41]
	v_mfma_f32_16x16x32_bf16 v[18:21], v[148:151], v[214:217], v[18:21]
	v_mfma_f32_16x16x32_bf16 v[26:29], v[158:161], v[214:217], v[26:29]
	v_mfma_f32_16x16x32_bf16 v[2:5], v[148:151], v[222:225], v[2:5]
	v_mfma_f32_16x16x32_bf16 v[6:9], v[158:161], v[222:225], v[6:9]
	v_mfma_f32_16x16x32_bf16 v[50:53], v[152:155], v[202:205], v[50:53]
	v_mfma_f32_16x16x32_bf16 v[62:65], v[166:169], v[202:205], v[62:65]
	v_mfma_f32_16x16x32_bf16 v[34:37], v[152:155], v[210:213], v[34:37]
	v_mfma_f32_16x16x32_bf16 v[38:41], v[166:169], v[210:213], v[38:41]
	v_mfma_f32_16x16x32_bf16 v[18:21], v[152:155], v[218:221], v[18:21]
	v_mfma_f32_16x16x32_bf16 v[26:29], v[166:169], v[218:221], v[26:29]
	v_mfma_f32_16x16x32_bf16 v[2:5], v[152:155], v[226:229], v[2:5]
	v_mfma_f32_16x16x32_bf16 v[6:9], v[166:169], v[226:229], v[6:9]
	s_setprio 0
	s_setprio 1
	v_mfma_f32_16x16x32_bf16 v[54:57], v[170:173], v[198:201], v[54:57]
	v_mfma_f32_16x16x32_bf16 v[66:69], v[178:181], v[198:201], v[66:69]
	v_mfma_f32_16x16x32_bf16 v[42:45], v[170:173], v[206:209], v[42:45]
	v_mfma_f32_16x16x32_bf16 v[46:49], v[178:181], v[206:209], v[46:49]
	v_mfma_f32_16x16x32_bf16 v[22:25], v[170:173], v[214:217], v[22:25]
	v_mfma_f32_16x16x32_bf16 v[30:33], v[178:181], v[214:217], v[30:33]
	v_mfma_f32_16x16x32_bf16 v[10:13], v[170:173], v[222:225], v[10:13]
	v_mfma_f32_16x16x32_bf16 v[14:17], v[178:181], v[222:225], v[14:17]
	v_mfma_f32_16x16x32_bf16 v[54:57], v[174:177], v[202:205], v[54:57]
	v_mfma_f32_16x16x32_bf16 v[66:69], v[194:197], v[202:205], v[66:69]
	v_mfma_f32_16x16x32_bf16 v[42:45], v[174:177], v[210:213], v[42:45]
	v_mfma_f32_16x16x32_bf16 v[46:49], v[194:197], v[210:213], v[46:49]
	v_mfma_f32_16x16x32_bf16 v[22:25], v[174:177], v[218:221], v[22:25]
	v_mfma_f32_16x16x32_bf16 v[30:33], v[194:197], v[218:221], v[30:33]
	v_mfma_f32_16x16x32_bf16 v[10:13], v[174:177], v[226:229], v[10:13]
	v_mfma_f32_16x16x32_bf16 v[14:17], v[194:197], v[226:229], v[14:17]
	s_setprio 0
	s_barrier
	s_add_i32 s64, s64, 2
	s_add_u32 s52, s52, 0x10000
	s_addc_u32 s53, s53, 0
	s_add_u32 s49, s49, 0x10000
	s_addc_u32 s63, s63, 0
	s_cmp_gt_u32 s64, 29
	s_cbranch_scc0 .LBB0_1079
	s_and_b64 vcc, exec, s[10:11]
	s_cbranch_vccz .LBB0_1082
	s_barrier

.LBB0_1230:
	s_add_u32 s16, s46, 0x4000
	s_addc_u32 s17, s47, 0
	s_cmp_eq_u32 s64, 28
	s_cselect_b32 s52, s60, s16
	s_cselect_b32 s53, s29, s17
	s_cselect_b32 s51, s27, s63
	s_cselect_b32 s50, s61, s62
	s_add_u32 s48, s52, 0x8000
	s_addc_u32 s49, s53, 0
	s_add_i32 s16, 0, 0x10000
	v_add_u32_e32 v144, s16, v1
	s_add_i32 s65, 0, 0x14000
	ds_read_b128 v[148:151], v144
	ds_read_b128 v[152:155], v144 offset:1024
	ds_read_b128 v[158:161], v144 offset:2048
	ds_read_b128 v[166:169], v144 offset:3072
	v_add_u32_e32 v144, s65, v1
	ds_read_b128 v[170:173], v144
	ds_read_b128 v[174:177], v144 offset:1024
	ds_read_b128 v[178:181], v144 offset:2048
	ds_read_b128 v[194:197], v144 offset:3072
	s_add_i32 m0, s20, 0xc000
	ds_read_b128 v[198:201], v147
	ds_read_b128 v[202:205], v147 offset:1024
	ds_read_b128 v[206:209], v147 offset:2048
	ds_read_b128 v[210:213], v147 offset:3072
	ds_read_b128 v[214:217], v147 offset:4096
	ds_read_b128 v[218:221], v147 offset:5120
	ds_read_b128 v[222:225], v147 offset:6144
	ds_read_b128 v[226:229], v147 offset:7168
	s_cmp_lg_u32 s32, 0
	s_cbranch_scc1 .Lrx_relu2_skip
	global_load_lds_dwordx4 v140, s[46:47]
	s_add_i32 m0, s20, 0xe000
	s_nop 0
	global_load_lds_dwordx4 v142, s[46:47]

.Lrx_relu2_w0:
	s_waitcnt vmcnt(24)
	s_waitcnt lgkmcnt(0)
	s_barrier
	s_setprio 1
	s_waitcnt lgkmcnt(0)
	v_mfma_f32_16x16x32_bf16 v[128:131], v[148:151], v[198:201], v[128:131]
	v_mfma_f32_16x16x32_bf16 v[124:127], v[158:161], v[198:201], v[124:127]
	v_mfma_f32_16x16x32_bf16 v[110:113], v[148:151], v[206:209], v[110:113]
	v_mfma_f32_16x16x32_bf16 v[106:109], v[158:161], v[206:209], v[106:109]
	v_mfma_f32_16x16x32_bf16 v[94:97], v[148:151], v[214:217], v[94:97]
	v_mfma_f32_16x16x32_bf16 v[90:93], v[158:161], v[214:217], v[90:93]
	v_mfma_f32_16x16x32_bf16 v[78:81], v[148:151], v[222:225], v[78:81]
	v_mfma_f32_16x16x32_bf16 v[74:77], v[158:161], v[222:225], v[74:77]
	v_mfma_f32_16x16x32_bf16 v[128:131], v[152:155], v[202:205], v[128:131]
	v_mfma_f32_16x16x32_bf16 v[124:127], v[166:169], v[202:205], v[124:127]
	v_mfma_f32_16x16x32_bf16 v[110:113], v[152:155], v[210:213], v[110:113]
	v_mfma_f32_16x16x32_bf16 v[106:109], v[166:169], v[210:213], v[106:109]
	v_mfma_f32_16x16x32_bf16 v[94:97], v[152:155], v[218:221], v[94:97]
	v_mfma_f32_16x16x32_bf16 v[90:93], v[166:169], v[218:221], v[90:93]
	v_mfma_f32_16x16x32_bf16 v[78:81], v[152:155], v[226:229], v[78:81]
	v_mfma_f32_16x16x32_bf16 v[74:77], v[166:169], v[226:229], v[74:77]
	s_setprio 0
	s_setprio 1
	v_mfma_f32_16x16x32_bf16 v[120:123], v[170:173], v[198:201], v[120:123]
	v_mfma_f32_16x16x32_bf16 v[116:119], v[178:181], v[198:201], v[116:119]
	v_mfma_f32_16x16x32_bf16 v[102:105], v[170:173], v[206:209], v[102:105]
	v_mfma_f32_16x16x32_bf16 v[98:101], v[178:181], v[206:209], v[98:101]
	v_mfma_f32_16x16x32_bf16 v[86:89], v[170:173], v[214:217], v[86:89]
	v_mfma_f32_16x16x32_bf16 v[82:85], v[178:181], v[214:217], v[82:85]
	v_mfma_f32_16x16x32_bf16 v[70:73], v[170:173], v[222:225], v[70:73]
	v_mfma_f32_16x16x32_bf16 v[66:69], v[178:181], v[222:225], v[66:69]
	v_mfma_f32_16x16x32_bf16 v[120:123], v[174:177], v[202:205], v[120:123]
	v_mfma_f32_16x16x32_bf16 v[116:119], v[194:197], v[202:205], v[116:119]
	v_mfma_f32_16x16x32_bf16 v[102:105], v[174:177], v[210:213], v[102:105]
	v_mfma_f32_16x16x32_bf16 v[98:101], v[194:197], v[210:213], v[98:101]
	v_mfma_f32_16x16x32_bf16 v[86:89], v[174:177], v[218:221], v[86:89]
	v_mfma_f32_16x16x32_bf16 v[82:85], v[194:197], v[218:221], v[82:85]
	v_mfma_f32_16x16x32_bf16 v[70:73], v[174:177], v[226:229], v[70:73]
	v_mfma_f32_16x16x32_bf16 v[66:69], v[194:197], v[226:229], v[66:69]
	s_setprio 0
	s_barrier
	s_add_i32 s16, s16, s7
	s_mov_b32 m0, s16
	ds_read_b128 v[198:201], v147 offset:16384
	ds_read_b128 v[202:205], v147 offset:17408
	ds_read_b128 v[206:209], v147 offset:18432
	ds_read_b128 v[210:213], v147 offset:19456
	ds_read_b128 v[214:217], v147 offset:20480
	ds_read_b128 v[218:221], v147 offset:21504
	ds_read_b128 v[222:225], v147 offset:22528
	ds_read_b128 v[226:229], v147 offset:23552
	global_load_lds_dwordx4 v114, s[50:51]
	s_add_i32 m0, s16, 0x2000
	s_add_u32 s16, s50, 0x1000
	s_addc_u32 s17, s51, 0
	s_add_i32 s65, s65, s7
	global_load_lds_dwordx4 v136, s[50:51]
	s_mov_b32 m0, s65
	s_nop 0
	global_load_lds_dwordx4 v114, s[16:17]
	s_add_i32 m0, s65, 0x2000
	s_nop 0
	global_load_lds_dwordx4 v136, s[16:17]
	s_mov_b32 m0, s20
	s_nop 0
	global_load_lds_dwordx4 v132, s[52:53]
	s_mov_b32 m0, s21
	s_nop 0
	global_load_lds_dwordx4 v134, s[52:53]
	s_cmp_lg_u32 s32, 0
	s_cbranch_scc1 .Lrx_relu2_w1
	s_waitcnt vmcnt(8)
.Lrx_relu2_w1:
	s_waitcnt vmcnt(24)
	s_waitcnt lgkmcnt(0)
	s_barrier
	s_setprio 1
	s_waitcnt lgkmcnt(0)
	v_mfma_f32_16x16x32_bf16 v[62:65], v[148:151], v[198:201], v[62:65]
	v_mfma_f32_16x16x32_bf16 v[58:61], v[158:161], v[198:201], v[58:61]
	v_mfma_f32_16x16x32_bf16 v[46:49], v[148:151], v[206:209], v[46:49]
	v_mfma_f32_16x16x32_bf16 v[42:45], v[158:161], v[206:209], v[42:45]
	v_mfma_f32_16x16x32_bf16 v[30:33], v[148:151], v[214:217], v[30:33]
	v_mfma_f32_16x16x32_bf16 v[26:29], v[158:161], v[214:217], v[26:29]
	v_mfma_f32_16x16x32_bf16 v[14:17], v[148:151], v[222:225], v[14:17]
	v_mfma_f32_16x16x32_bf16 v[10:13], v[158:161], v[222:225], v[10:13]
	v_mfma_f32_16x16x32_bf16 v[62:65], v[152:155], v[202:205], v[62:65]
	v_mfma_f32_16x16x32_bf16 v[58:61], v[166:169], v[202:205], v[58:61]
	v_mfma_f32_16x16x32_bf16 v[46:49], v[152:155], v[210:213], v[46:49]
	v_mfma_f32_16x16x32_bf16 v[42:45], v[166:169], v[210:213], v[42:45]
	v_mfma_f32_16x16x32_bf16 v[30:33], v[152:155], v[218:221], v[30:33]
	v_mfma_f32_16x16x32_bf16 v[26:29], v[166:169], v[218:221], v[26:29]
	v_mfma_f32_16x16x32_bf16 v[14:17], v[152:155], v[226:229], v[14:17]
	v_mfma_f32_16x16x32_bf16 v[10:13], v[166:169], v[226:229], v[10:13]
	s_setprio 0
	s_setprio 1
	v_mfma_f32_16x16x32_bf16 v[54:57], v[170:173], v[198:201], v[54:57]
	v_mfma_f32_16x16x32_bf16 v[50:53], v[178:181], v[198:201], v[50:53]
	v_mfma_f32_16x16x32_bf16 v[38:41], v[170:173], v[206:209], v[38:41]
	v_mfma_f32_16x16x32_bf16 v[34:37], v[178:181], v[206:209], v[34:37]
	v_mfma_f32_16x16x32_bf16 v[22:25], v[170:173], v[214:217], v[22:25]
	v_mfma_f32_16x16x32_bf16 v[18:21], v[178:181], v[214:217], v[18:21]
	v_mfma_f32_16x16x32_bf16 v[6:9], v[170:173], v[222:225], v[6:9]
	v_mfma_f32_16x16x32_bf16 v[2:5], v[178:181], v[222:225], v[2:5]
	v_mfma_f32_16x16x32_bf16 v[54:57], v[174:177], v[202:205], v[54:57]
	v_mfma_f32_16x16x32_bf16 v[50:53], v[194:197], v[202:205], v[50:53]
	v_mfma_f32_16x16x32_bf16 v[38:41], v[174:177], v[210:213], v[38:41]
	v_mfma_f32_16x16x32_bf16 v[34:37], v[194:197], v[210:213], v[34:37]
	v_mfma_f32_16x16x32_bf16 v[22:25], v[174:177], v[218:221], v[22:25]
	v_mfma_f32_16x16x32_bf16 v[18:21], v[194:197], v[218:221], v[18:21]
	v_mfma_f32_16x16x32_bf16 v[6:9], v[174:177], v[226:229], v[6:9]
	v_mfma_f32_16x16x32_bf16 v[2:5], v[194:197], v[226:229], v[2:5]
	s_setprio 0
	s_barrier
	s_add_i32 s65, 0, 0x18000
	v_add_u32_e32 v144, s65, v1
	s_add_i32 s66, 0, 0x1c000
	ds_read_b128 v[148:151], v144
	ds_read_b128 v[152:155], v144 offset:1024
	ds_read_b128 v[158:161], v144 offset:2048
	ds_read_b128 v[166:169], v144 offset:3072
	v_add_u32_e32 v144, s66, v1
	ds_read_b128 v[170:173], v144
	ds_read_b128 v[174:177], v144 offset:1024
	ds_read_b128 v[178:181], v144 offset:2048
	ds_read_b128 v[194:197], v144 offset:3072
	s_add_u32 s16, s52, 0x4000
	s_addc_u32 s17, s53, 0
	s_mov_b32 m0, s24
	ds_read_b128 v[198:201], v147 offset:32768
	ds_read_b128 v[202:205], v147 offset:33792
	ds_read_b128 v[206:209], v147 offset:34816
	ds_read_b128 v[210:213], v147 offset:35840
	ds_read_b128 v[214:217], v147 offset:36864
	ds_read_b128 v[218:221], v147 offset:37888
	ds_read_b128 v[222:225], v147 offset:38912
	ds_read_b128 v[226:229], v147 offset:39936
	global_load_lds_dwordx4 v132, s[16:17]
	s_mov_b32 m0, s37
	s_nop 0
	global_load_lds_dwordx4 v134, s[16:17]
	s_cmp_lg_u32 s32, 0
	s_cbranch_scc1 .Lrx_relu2_w2
	s_waitcnt vmcnt(8)
.Lrx_relu2_w2:
	s_waitcnt vmcnt(24)
	s_mov_b32 s32, 0
	s_waitcnt lgkmcnt(0)
	s_barrier
	s_setprio 1
	s_waitcnt lgkmcnt(0)
	v_mfma_f32_16x16x32_bf16 v[128:131], v[148:151], v[198:201], v[128:131]
	v_mfma_f32_16x16x32_bf16 v[124:127], v[158:161], v[198:201], v[124:127]
	v_mfma_f32_16x16x32_bf16 v[110:113], v[148:151], v[206:209], v[110:113]
	v_mfma_f32_16x16x32_bf16 v[106:109], v[158:161], v[206:209], v[106:109]
	v_mfma_f32_16x16x32_bf16 v[94:97], v[148:151], v[214:217], v[94:97]
	v_mfma_f32_16x16x32_bf16 v[90:93], v[158:161], v[214:217], v[90:93]
	v_mfma_f32_16x16x32_bf16 v[78:81], v[148:151], v[222:225], v[78:81]
	v_mfma_f32_16x16x32_bf16 v[74:77], v[158:161], v[222:225], v[74:77]
	v_mfma_f32_16x16x32_bf16 v[128:131], v[152:155], v[202:205], v[128:131]
	v_mfma_f32_16x16x32_bf16 v[124:127], v[166:169], v[202:205], v[124:127]
	v_mfma_f32_16x16x32_bf16 v[110:113], v[152:155], v[210:213], v[110:113]
	v_mfma_f32_16x16x32_bf16 v[106:109], v[166:169], v[210:213], v[106:109]
	v_mfma_f32_16x16x32_bf16 v[94:97], v[152:155], v[218:221], v[94:97]
	v_mfma_f32_16x16x32_bf16 v[90:93], v[166:169], v[218:221], v[90:93]
	v_mfma_f32_16x16x32_bf16 v[78:81], v[152:155], v[226:229], v[78:81]
	v_mfma_f32_16x16x32_bf16 v[74:77], v[166:169], v[226:229], v[74:77]
	s_setprio 0
	s_setprio 1
	v_mfma_f32_16x16x32_bf16 v[120:123], v[170:173], v[198:201], v[120:123]
	v_mfma_f32_16x16x32_bf16 v[116:119], v[178:181], v[198:201], v[116:119]
	v_mfma_f32_16x16x32_bf16 v[102:105], v[170:173], v[206:209], v[102:105]
	v_mfma_f32_16x16x32_bf16 v[98:101], v[178:181], v[206:209], v[98:101]
	v_mfma_f32_16x16x32_bf16 v[86:89], v[170:173], v[214:217], v[86:89]
	v_mfma_f32_16x16x32_bf16 v[82:85], v[178:181], v[214:217], v[82:85]
	v_mfma_f32_16x16x32_bf16 v[70:73], v[170:173], v[222:225], v[70:73]
	v_mfma_f32_16x16x32_bf16 v[66:69], v[178:181], v[222:225], v[66:69]
	v_mfma_f32_16x16x32_bf16 v[120:123], v[174:177], v[202:205], v[120:123]
	v_mfma_f32_16x16x32_bf16 v[116:119], v[194:197], v[202:205], v[116:119]
	v_mfma_f32_16x16x32_bf16 v[102:105], v[174:177], v[210:213], v[102:105]
	v_mfma_f32_16x16x32_bf16 v[98:101], v[194:197], v[210:213], v[98:101]
	v_mfma_f32_16x16x32_bf16 v[86:89], v[174:177], v[218:221], v[86:89]
	v_mfma_f32_16x16x32_bf16 v[82:85], v[194:197], v[218:221], v[82:85]
	v_mfma_f32_16x16x32_bf16 v[70:73], v[174:177], v[226:229], v[70:73]
	v_mfma_f32_16x16x32_bf16 v[66:69], v[194:197], v[226:229], v[66:69]
	s_setprio 0
	s_barrier
	s_add_u32 s16, s50, 0x8000
	s_addc_u32 s17, s51, 0
	s_add_i32 s52, s65, s7
	s_mov_b32 m0, s52
	ds_read_b128 v[198:201], v147 offset:49152
	ds_read_b128 v[202:205], v147 offset:50176
	ds_read_b128 v[206:209], v147 offset:51200
	ds_read_b128 v[210:213], v147 offset:52224
	ds_read_b128 v[214:217], v147 offset:53248
	ds_read_b128 v[218:221], v147 offset:54272
	ds_read_b128 v[222:225], v147 offset:55296
	ds_read_b128 v[226:229], v147 offset:56320
	global_load_lds_dwordx4 v114, s[16:17]
	s_add_i32 m0, s52, 0x2000
	v_lshl_add_u64 v[144:145], s[16:17], 0, v[136:137]
	s_add_u32 s16, s50, 0x9000
	s_addc_u32 s17, s51, 0
	s_add_i32 s50, s66, s7
	global_load_lds_dwordx4 v[144:145], off
	s_mov_b32 m0, s50
	s_nop 0
	global_load_lds_dwordx4 v114, s[16:17]
	s_add_i32 m0, s50, 0x2000
	s_nop 0
	global_load_lds_dwordx4 v136, s[16:17]
	s_mov_b32 m0, s54
	s_nop 0
	global_load_lds_dwordx4 v132, s[48:49]
	s_mov_b32 m0, s55
	s_nop 0
	global_load_lds_dwordx4 v134, s[48:49]
	s_waitcnt vmcnt(8)
	s_waitcnt lgkmcnt(0)
	s_barrier
	s_setprio 1
	s_waitcnt lgkmcnt(0)
	v_mfma_f32_16x16x32_bf16 v[62:65], v[148:151], v[198:201], v[62:65]
	v_mfma_f32_16x16x32_bf16 v[58:61], v[158:161], v[198:201], v[58:61]
	v_mfma_f32_16x16x32_bf16 v[46:49], v[148:151], v[206:209], v[46:49]
	v_mfma_f32_16x16x32_bf16 v[42:45], v[158:161], v[206:209], v[42:45]
	v_mfma_f32_16x16x32_bf16 v[30:33], v[148:151], v[214:217], v[30:33]
	v_mfma_f32_16x16x32_bf16 v[26:29], v[158:161], v[214:217], v[26:29]
	v_mfma_f32_16x16x32_bf16 v[14:17], v[148:151], v[222:225], v[14:17]
	v_mfma_f32_16x16x32_bf16 v[10:13], v[158:161], v[222:225], v[10:13]
	v_mfma_f32_16x16x32_bf16 v[62:65], v[152:155], v[202:205], v[62:65]
	v_mfma_f32_16x16x32_bf16 v[58:61], v[166:169], v[202:205], v[58:61]
	v_mfma_f32_16x16x32_bf16 v[46:49], v[152:155], v[210:213], v[46:49]
	v_mfma_f32_16x16x32_bf16 v[42:45], v[166:169], v[210:213], v[42:45]
	v_mfma_f32_16x16x32_bf16 v[30:33], v[152:155], v[218:221], v[30:33]
	v_mfma_f32_16x16x32_bf16 v[26:29], v[166:169], v[218:221], v[26:29]
	v_mfma_f32_16x16x32_bf16 v[14:17], v[152:155], v[226:229], v[14:17]
	v_mfma_f32_16x16x32_bf16 v[10:13], v[166:169], v[226:229], v[10:13]
	s_setprio 0
	s_setprio 1
	v_mfma_f32_16x16x32_bf16 v[54:57], v[170:173], v[198:201], v[54:57]
	v_mfma_f32_16x16x32_bf16 v[50:53], v[178:181], v[198:201], v[50:53]
	v_mfma_f32_16x16x32_bf16 v[38:41], v[170:173], v[206:209], v[38:41]
	v_mfma_f32_16x16x32_bf16 v[34:37], v[178:181], v[206:209], v[34:37]
	v_mfma_f32_16x16x32_bf16 v[22:25], v[170:173], v[214:217], v[22:25]
	v_mfma_f32_16x16x32_bf16 v[18:21], v[178:181], v[214:217], v[18:21]
	v_mfma_f32_16x16x32_bf16 v[6:9], v[170:173], v[222:225], v[6:9]
	v_mfma_f32_16x16x32_bf16 v[2:5], v[178:181], v[222:225], v[2:5]
	v_mfma_f32_16x16x32_bf16 v[54:57], v[174:177], v[202:205], v[54:57]
	v_mfma_f32_16x16x32_bf16 v[50:53], v[194:197], v[202:205], v[50:53]
	v_mfma_f32_16x16x32_bf16 v[38:41], v[174:177], v[210:213], v[38:41]
	v_mfma_f32_16x16x32_bf16 v[34:37], v[194:197], v[210:213], v[34:37]
	v_mfma_f32_16x16x32_bf16 v[22:25], v[174:177], v[218:221], v[22:25]
	v_mfma_f32_16x16x32_bf16 v[18:21], v[194:197], v[218:221], v[18:21]
	v_mfma_f32_16x16x32_bf16 v[6:9], v[174:177], v[226:229], v[6:9]
	v_mfma_f32_16x16x32_bf16 v[2:5], v[194:197], v[226:229], v[2:5]
	s_setprio 0
	s_barrier
	s_add_i32 s64, s64, 2
	s_add_u32 s46, s46, 0x10000
	s_addc_u32 s47, s47, 0
	s_add_u32 s62, s62, 0x10000
	s_addc_u32 s63, s63, 0
	s_cmp_gt_u32 s64, 29
	s_cbranch_scc0 .LBB0_1230
	s_add_u32 s100, s60, 0xc000
	s_addc_u32 s101, s29, 0
	v_lshl_add_u64 v[144:145], s[100:101], 0, v[140:141]
	s_add_i32 m0, s20, 0xc000
	s_nop 0
	global_load_lds_dwordx4 v[144:145], off
	v_lshl_add_u64 v[144:145], s[100:101], 0, v[142:143]
	s_add_i32 m0, s20, 0xe000
	s_nop 0
	global_load_lds_dwordx4 v[144:145], off
	s_and_b64 vcc, exec, s[10:11]
	s_cbranch_vccz .LBB0_1233
	s_barrier

.LBB0_1334:
	s_add_u32 s16, s52, 0x4000
	s_addc_u32 s17, s53, 0
	s_cmpk_eq_i32 s66, 0x7c
	s_cselect_b32 s56, s29, s16
	s_cselect_b32 s57, s24, s17
	s_cselect_b32 s55, s27, s65
	s_cselect_b32 s54, s47, s49
	s_add_u32 s50, s56, 0x8000
	s_addc_u32 s51, s57, 0
	s_add_i32 s16, 0, 0x10000
	v_add_u32_e32 v144, s16, v146
	s_add_i32 s67, 0, 0x14000
	ds_read_b128 v[148:151], v144
	ds_read_b128 v[152:155], v144 offset:1024
	ds_read_b128 v[158:161], v144 offset:2048
	ds_read_b128 v[166:169], v144 offset:3072
	v_add_u32_e32 v144, s67, v146
	ds_read_b128 v[170:173], v144
	ds_read_b128 v[174:177], v144 offset:1024
	ds_read_b128 v[178:181], v144 offset:2048
	ds_read_b128 v[194:197], v144 offset:3072
	s_add_i32 m0, s37, 0xc000
	ds_read_b128 v[198:201], v147
	ds_read_b128 v[202:205], v147 offset:1024
	ds_read_b128 v[206:209], v147 offset:2048
	ds_read_b128 v[210:213], v147 offset:3072
	ds_read_b128 v[214:217], v147 offset:4096
	ds_read_b128 v[218:221], v147 offset:5120
	ds_read_b128 v[222:225], v147 offset:6144
	ds_read_b128 v[226:229], v147 offset:7168
	global_load_lds_dwordx4 v140, s[52:53]
	s_add_i32 m0, s37, 0xe000
	s_nop 0
	global_load_lds_dwordx4 v142, s[52:53]
	s_waitcnt vmcnt(8)
	s_waitcnt lgkmcnt(0)
	s_barrier
	s_setprio 1
	s_waitcnt lgkmcnt(0)
	v_mfma_f32_16x16x32_bf16 v[116:119], v[148:151], v[198:201], v[116:119]
	v_mfma_f32_16x16x32_bf16 v[124:127], v[158:161], v[198:201], v[124:127]
	v_mfma_f32_16x16x32_bf16 v[98:101], v[148:151], v[206:209], v[98:101]
	v_mfma_f32_16x16x32_bf16 v[102:105], v[158:161], v[206:209], v[102:105]
	v_mfma_f32_16x16x32_bf16 v[82:85], v[148:151], v[214:217], v[82:85]
	v_mfma_f32_16x16x32_bf16 v[90:93], v[158:161], v[214:217], v[90:93]
	v_mfma_f32_16x16x32_bf16 v[58:61], v[148:151], v[222:225], v[58:61]
	v_mfma_f32_16x16x32_bf16 v[70:73], v[158:161], v[222:225], v[70:73]
	v_mfma_f32_16x16x32_bf16 v[116:119], v[152:155], v[202:205], v[116:119]
	v_mfma_f32_16x16x32_bf16 v[124:127], v[166:169], v[202:205], v[124:127]
	v_mfma_f32_16x16x32_bf16 v[98:101], v[152:155], v[210:213], v[98:101]
	v_mfma_f32_16x16x32_bf16 v[102:105], v[166:169], v[210:213], v[102:105]
	v_mfma_f32_16x16x32_bf16 v[82:85], v[152:155], v[218:221], v[82:85]
	v_mfma_f32_16x16x32_bf16 v[90:93], v[166:169], v[218:221], v[90:93]
	v_mfma_f32_16x16x32_bf16 v[58:61], v[152:155], v[226:229], v[58:61]
	v_mfma_f32_16x16x32_bf16 v[70:73], v[166:169], v[226:229], v[70:73]
	s_setprio 0
	s_setprio 1
	v_mfma_f32_16x16x32_bf16 v[120:123], v[170:173], v[198:201], v[120:123]
	v_mfma_f32_16x16x32_bf16 v[128:131], v[178:181], v[198:201], v[128:131]
	v_mfma_f32_16x16x32_bf16 v[106:109], v[170:173], v[206:209], v[106:109]
	v_mfma_f32_16x16x32_bf16 v[110:113], v[178:181], v[206:209], v[110:113]
	v_mfma_f32_16x16x32_bf16 v[86:89], v[170:173], v[214:217], v[86:89]
	v_mfma_f32_16x16x32_bf16 v[94:97], v[178:181], v[214:217], v[94:97]
	v_mfma_f32_16x16x32_bf16 v[74:77], v[170:173], v[222:225], v[74:77]
	v_mfma_f32_16x16x32_bf16 v[78:81], v[178:181], v[222:225], v[78:81]
	v_mfma_f32_16x16x32_bf16 v[120:123], v[174:177], v[202:205], v[120:123]
	v_mfma_f32_16x16x32_bf16 v[128:131], v[194:197], v[202:205], v[128:131]
	v_mfma_f32_16x16x32_bf16 v[106:109], v[174:177], v[210:213], v[106:109]
	v_mfma_f32_16x16x32_bf16 v[110:113], v[194:197], v[210:213], v[110:113]
	v_mfma_f32_16x16x32_bf16 v[86:89], v[174:177], v[218:221], v[86:89]
	v_mfma_f32_16x16x32_bf16 v[94:97], v[194:197], v[218:221], v[94:97]
	v_mfma_f32_16x16x32_bf16 v[74:77], v[174:177], v[226:229], v[74:77]
	v_mfma_f32_16x16x32_bf16 v[78:81], v[194:197], v[226:229], v[78:81]
	s_setprio 0
	s_barrier
	s_add_i32 s16, s16, s15
	s_mov_b32 m0, s16
	ds_read_b128 v[198:201], v147 offset:16384
	ds_read_b128 v[202:205], v147 offset:17408
	ds_read_b128 v[206:209], v147 offset:18432
	ds_read_b128 v[210:213], v147 offset:19456
	ds_read_b128 v[214:217], v147 offset:20480
	ds_read_b128 v[218:221], v147 offset:21504
	ds_read_b128 v[222:225], v147 offset:22528
	ds_read_b128 v[226:229], v147 offset:23552
	global_load_lds_dwordx4 v114, s[54:55]
	s_add_i32 m0, s16, 0x2000
	s_add_u32 s16, s54, 0x1000
	s_addc_u32 s17, s55, 0
	s_add_i32 s67, s67, s15
	global_load_lds_dwordx4 v136, s[54:55]
	s_mov_b32 m0, s67
	s_nop 0
	global_load_lds_dwordx4 v114, s[16:17]
	s_add_i32 m0, s67, 0x2000
	s_nop 0
	global_load_lds_dwordx4 v136, s[16:17]
	s_mov_b32 m0, s37
	s_nop 0
	global_load_lds_dwordx4 v132, s[56:57]
	s_mov_b32 m0, s58
	s_nop 0
	global_load_lds_dwordx4 v134, s[56:57]
	s_waitcnt vmcnt(8)
	s_waitcnt lgkmcnt(0)
	s_barrier
	s_setprio 1
	s_waitcnt lgkmcnt(0)
	v_mfma_f32_16x16x32_bf16 v[50:53], v[148:151], v[198:201], v[50:53]
	v_mfma_f32_16x16x32_bf16 v[62:65], v[158:161], v[198:201], v[62:65]
	v_mfma_f32_16x16x32_bf16 v[34:37], v[148:151], v[206:209], v[34:37]
	v_mfma_f32_16x16x32_bf16 v[38:41], v[158:161], v[206:209], v[38:41]
	v_mfma_f32_16x16x32_bf16 v[18:21], v[148:151], v[214:217], v[18:21]
	v_mfma_f32_16x16x32_bf16 v[26:29], v[158:161], v[214:217], v[26:29]
	v_mfma_f32_16x16x32_bf16 v[2:5], v[148:151], v[222:225], v[2:5]
	v_mfma_f32_16x16x32_bf16 v[6:9], v[158:161], v[222:225], v[6:9]
	v_mfma_f32_16x16x32_bf16 v[50:53], v[152:155], v[202:205], v[50:53]
	v_mfma_f32_16x16x32_bf16 v[62:65], v[166:169], v[202:205], v[62:65]
	v_mfma_f32_16x16x32_bf16 v[34:37], v[152:155], v[210:213], v[34:37]
	v_mfma_f32_16x16x32_bf16 v[38:41], v[166:169], v[210:213], v[38:41]
	v_mfma_f32_16x16x32_bf16 v[18:21], v[152:155], v[218:221], v[18:21]
	v_mfma_f32_16x16x32_bf16 v[26:29], v[166:169], v[218:221], v[26:29]
	v_mfma_f32_16x16x32_bf16 v[2:5], v[152:155], v[226:229], v[2:5]
	v_mfma_f32_16x16x32_bf16 v[6:9], v[166:169], v[226:229], v[6:9]
	s_setprio 0
	s_setprio 1
	v_mfma_f32_16x16x32_bf16 v[54:57], v[170:173], v[198:201], v[54:57]
	v_mfma_f32_16x16x32_bf16 v[66:69], v[178:181], v[198:201], v[66:69]
	v_mfma_f32_16x16x32_bf16 v[42:45], v[170:173], v[206:209], v[42:45]
	v_mfma_f32_16x16x32_bf16 v[46:49], v[178:181], v[206:209], v[46:49]
	v_mfma_f32_16x16x32_bf16 v[22:25], v[170:173], v[214:217], v[22:25]
	v_mfma_f32_16x16x32_bf16 v[30:33], v[178:181], v[214:217], v[30:33]
	v_mfma_f32_16x16x32_bf16 v[10:13], v[170:173], v[222:225], v[10:13]
	v_mfma_f32_16x16x32_bf16 v[14:17], v[178:181], v[222:225], v[14:17]
	v_mfma_f32_16x16x32_bf16 v[54:57], v[174:177], v[202:205], v[54:57]
	v_mfma_f32_16x16x32_bf16 v[66:69], v[194:197], v[202:205], v[66:69]
	v_mfma_f32_16x16x32_bf16 v[42:45], v[174:177], v[210:213], v[42:45]
	v_mfma_f32_16x16x32_bf16 v[46:49], v[194:197], v[210:213], v[46:49]
	v_mfma_f32_16x16x32_bf16 v[22:25], v[174:177], v[218:221], v[22:25]
	v_mfma_f32_16x16x32_bf16 v[30:33], v[194:197], v[218:221], v[30:33]
	v_mfma_f32_16x16x32_bf16 v[10:13], v[174:177], v[226:229], v[10:13]
	v_mfma_f32_16x16x32_bf16 v[14:17], v[194:197], v[226:229], v[14:17]
	s_setprio 0
	s_barrier
	s_add_i32 s67, 0, 0x18000
	v_add_u32_e32 v144, s67, v146
	s_add_i32 s68, 0, 0x1c000
	ds_read_b128 v[148:151], v144
	ds_read_b128 v[152:155], v144 offset:1024
	ds_read_b128 v[158:161], v144 offset:2048
	ds_read_b128 v[166:169], v144 offset:3072
	v_add_u32_e32 v144, s68, v146
	ds_read_b128 v[170:173], v144
	ds_read_b128 v[174:177], v144 offset:1024
	ds_read_b128 v[178:181], v144 offset:2048
	ds_read_b128 v[194:197], v144 offset:3072
	s_add_u32 s16, s56, 0x4000
	s_addc_u32 s17, s57, 0
	s_mov_b32 m0, s59
	ds_read_b128 v[198:201], v147 offset:32768
	ds_read_b128 v[202:205], v147 offset:33792
	ds_read_b128 v[206:209], v147 offset:34816
	ds_read_b128 v[210:213], v147 offset:35840
	ds_read_b128 v[214:217], v147 offset:36864
	ds_read_b128 v[218:221], v147 offset:37888
	ds_read_b128 v[222:225], v147 offset:38912
	ds_read_b128 v[226:229], v147 offset:39936
	global_load_lds_dwordx4 v132, s[16:17]
	s_mov_b32 m0, s60
	s_nop 0
	global_load_lds_dwordx4 v134, s[16:17]
	s_waitcnt vmcnt(8)
	s_waitcnt lgkmcnt(0)
	s_barrier
	s_setprio 1
	s_waitcnt lgkmcnt(0)
	v_mfma_f32_16x16x32_bf16 v[116:119], v[148:151], v[198:201], v[116:119]
	v_mfma_f32_16x16x32_bf16 v[124:127], v[158:161], v[198:201], v[124:127]
	v_mfma_f32_16x16x32_bf16 v[98:101], v[148:151], v[206:209], v[98:101]
	v_mfma_f32_16x16x32_bf16 v[102:105], v[158:161], v[206:209], v[102:105]
	v_mfma_f32_16x16x32_bf16 v[82:85], v[148:151], v[214:217], v[82:85]
	v_mfma_f32_16x16x32_bf16 v[90:93], v[158:161], v[214:217], v[90:93]
	v_mfma_f32_16x16x32_bf16 v[58:61], v[148:151], v[222:225], v[58:61]
	v_mfma_f32_16x16x32_bf16 v[70:73], v[158:161], v[222:225], v[70:73]
	v_mfma_f32_16x16x32_bf16 v[116:119], v[152:155], v[202:205], v[116:119]
	v_mfma_f32_16x16x32_bf16 v[124:127], v[166:169], v[202:205], v[124:127]
	v_mfma_f32_16x16x32_bf16 v[98:101], v[152:155], v[210:213], v[98:101]
	v_mfma_f32_16x16x32_bf16 v[102:105], v[166:169], v[210:213], v[102:105]
	v_mfma_f32_16x16x32_bf16 v[82:85], v[152:155], v[218:221], v[82:85]
	v_mfma_f32_16x16x32_bf16 v[90:93], v[166:169], v[218:221], v[90:93]
	v_mfma_f32_16x16x32_bf16 v[58:61], v[152:155], v[226:229], v[58:61]
	v_mfma_f32_16x16x32_bf16 v[70:73], v[166:169], v[226:229], v[70:73]
	s_setprio 0
	s_setprio 1
	v_mfma_f32_16x16x32_bf16 v[120:123], v[170:173], v[198:201], v[120:123]
	v_mfma_f32_16x16x32_bf16 v[128:131], v[178:181], v[198:201], v[128:131]
	v_mfma_f32_16x16x32_bf16 v[106:109], v[170:173], v[206:209], v[106:109]
	v_mfma_f32_16x16x32_bf16 v[110:113], v[178:181], v[206:209], v[110:113]
	v_mfma_f32_16x16x32_bf16 v[86:89], v[170:173], v[214:217], v[86:89]
	v_mfma_f32_16x16x32_bf16 v[94:97], v[178:181], v[214:217], v[94:97]
	v_mfma_f32_16x16x32_bf16 v[74:77], v[170:173], v[222:225], v[74:77]
	v_mfma_f32_16x16x32_bf16 v[78:81], v[178:181], v[222:225], v[78:81]
	v_mfma_f32_16x16x32_bf16 v[120:123], v[174:177], v[202:205], v[120:123]
	v_mfma_f32_16x16x32_bf16 v[128:131], v[194:197], v[202:205], v[128:131]
	v_mfma_f32_16x16x32_bf16 v[106:109], v[174:177], v[210:213], v[106:109]
	v_mfma_f32_16x16x32_bf16 v[110:113], v[194:197], v[210:213], v[110:113]
	v_mfma_f32_16x16x32_bf16 v[86:89], v[174:177], v[218:221], v[86:89]
	v_mfma_f32_16x16x32_bf16 v[94:97], v[194:197], v[218:221], v[94:97]
	v_mfma_f32_16x16x32_bf16 v[74:77], v[174:177], v[226:229], v[74:77]
	v_mfma_f32_16x16x32_bf16 v[78:81], v[194:197], v[226:229], v[78:81]
	s_setprio 0
	s_barrier
	s_add_u32 s16, s54, 0x8000
	s_addc_u32 s17, s55, 0
	s_add_i32 s56, s67, s15
	s_mov_b32 m0, s56
	ds_read_b128 v[198:201], v147 offset:49152
	ds_read_b128 v[202:205], v147 offset:50176
	ds_read_b128 v[206:209], v147 offset:51200
	ds_read_b128 v[210:213], v147 offset:52224
	ds_read_b128 v[214:217], v147 offset:53248
	ds_read_b128 v[218:221], v147 offset:54272
	ds_read_b128 v[222:225], v147 offset:55296
	ds_read_b128 v[226:229], v147 offset:56320
	global_load_lds_dwordx4 v114, s[16:17]
	s_add_i32 m0, s56, 0x2000
	v_lshl_add_u64 v[144:145], s[16:17], 0, v[136:137]
	s_add_u32 s16, s54, 0x9000
	s_addc_u32 s17, s55, 0
	s_add_i32 s54, s68, s15
	global_load_lds_dwordx4 v[144:145], off
	s_mov_b32 m0, s54
	s_nop 0
	global_load_lds_dwordx4 v114, s[16:17]
	s_add_i32 m0, s54, 0x2000
	s_nop 0
	global_load_lds_dwordx4 v136, s[16:17]
	s_mov_b32 m0, s61
	s_nop 0
	global_load_lds_dwordx4 v132, s[50:51]
	s_mov_b32 m0, s62
	s_nop 0
	global_load_lds_dwordx4 v134, s[50:51]
	s_waitcnt vmcnt(8)
	s_waitcnt lgkmcnt(0)
	s_barrier
	s_setprio 1
	s_waitcnt lgkmcnt(0)
	v_mfma_f32_16x16x32_bf16 v[50:53], v[148:151], v[198:201], v[50:53]
	v_mfma_f32_16x16x32_bf16 v[62:65], v[158:161], v[198:201], v[62:65]
	v_mfma_f32_16x16x32_bf16 v[34:37], v[148:151], v[206:209], v[34:37]
	v_mfma_f32_16x16x32_bf16 v[38:41], v[158:161], v[206:209], v[38:41]
	v_mfma_f32_16x16x32_bf16 v[18:21], v[148:151], v[214:217], v[18:21]
	v_mfma_f32_16x16x32_bf16 v[26:29], v[158:161], v[214:217], v[26:29]
	v_mfma_f32_16x16x32_bf16 v[2:5], v[148:151], v[222:225], v[2:5]
	v_mfma_f32_16x16x32_bf16 v[6:9], v[158:161], v[222:225], v[6:9]
	v_mfma_f32_16x16x32_bf16 v[50:53], v[152:155], v[202:205], v[50:53]
	v_mfma_f32_16x16x32_bf16 v[62:65], v[166:169], v[202:205], v[62:65]
	v_mfma_f32_16x16x32_bf16 v[34:37], v[152:155], v[210:213], v[34:37]
	v_mfma_f32_16x16x32_bf16 v[38:41], v[166:169], v[210:213], v[38:41]
	v_mfma_f32_16x16x32_bf16 v[18:21], v[152:155], v[218:221], v[18:21]
	v_mfma_f32_16x16x32_bf16 v[26:29], v[166:169], v[218:221], v[26:29]
	v_mfma_f32_16x16x32_bf16 v[2:5], v[152:155], v[226:229], v[2:5]
	v_mfma_f32_16x16x32_bf16 v[6:9], v[166:169], v[226:229], v[6:9]
	s_setprio 0
	s_setprio 1
	v_mfma_f32_16x16x32_bf16 v[54:57], v[170:173], v[198:201], v[54:57]
	v_mfma_f32_16x16x32_bf16 v[66:69], v[178:181], v[198:201], v[66:69]
	v_mfma_f32_16x16x32_bf16 v[42:45], v[170:173], v[206:209], v[42:45]
	v_mfma_f32_16x16x32_bf16 v[46:49], v[178:181], v[206:209], v[46:49]
	v_mfma_f32_16x16x32_bf16 v[22:25], v[170:173], v[214:217], v[22:25]
	v_mfma_f32_16x16x32_bf16 v[30:33], v[178:181], v[214:217], v[30:33]
	v_mfma_f32_16x16x32_bf16 v[10:13], v[170:173], v[222:225], v[10:13]
	v_mfma_f32_16x16x32_bf16 v[14:17], v[178:181], v[222:225], v[14:17]
	v_mfma_f32_16x16x32_bf16 v[54:57], v[174:177], v[202:205], v[54:57]
	v_mfma_f32_16x16x32_bf16 v[66:69], v[194:197], v[202:205], v[66:69]
	v_mfma_f32_16x16x32_bf16 v[42:45], v[174:177], v[210:213], v[42:45]
	v_mfma_f32_16x16x32_bf16 v[46:49], v[194:197], v[210:213], v[46:49]
	v_mfma_f32_16x16x32_bf16 v[22:25], v[174:177], v[218:221], v[22:25]
	v_mfma_f32_16x16x32_bf16 v[30:33], v[194:197], v[218:221], v[30:33]
	v_mfma_f32_16x16x32_bf16 v[10:13], v[174:177], v[226:229], v[10:13]
	v_mfma_f32_16x16x32_bf16 v[14:17], v[194:197], v[226:229], v[14:17]
	s_setprio 0
	s_barrier
	s_add_i32 s66, s66, 2
	s_add_u32 s52, s52, 0x10000
	s_addc_u32 s53, s53, 0
	s_add_u32 s49, s49, 0x10000
	s_addc_u32 s65, s65, 0
	s_cmpk_gt_u32 s66, 0x7d
	s_cbranch_scc0 .LBB0_1334
	s_and_b64 vcc, exec, s[10:11]
	s_cbranch_vccz .LBB0_1337
	s_barrier

.LBB0_1376:
	s_add_u32 s16, s44, 0x4000
	s_addc_u32 s17, s45, 0
	s_cmpk_eq_i32 s60, 0x7c
	s_cselect_b32 s48, s56, s16
	s_cselect_b32 s49, s11, s17
	s_cselect_b32 s47, s1, s59
	s_cselect_b32 s46, s57, s58
	s_add_u32 s42, s48, 0x8000
	s_addc_u32 s43, s49, 0
	s_add_i32 s16, 0, 0x10000
	v_add_u32_e32 v147, s16, v144
	s_add_i32 s61, 0, 0x14000
	ds_read_b128 v[148:151], v147
	ds_read_b128 v[152:155], v147 offset:1024
	ds_read_b128 v[158:161], v147 offset:2048
	ds_read_b128 v[166:169], v147 offset:3072
	v_add_u32_e32 v147, s61, v144
	ds_read_b128 v[170:173], v147
	ds_read_b128 v[174:177], v147 offset:1024
	ds_read_b128 v[178:181], v147 offset:2048
	ds_read_b128 v[194:197], v147 offset:3072
	s_add_i32 m0, s37, 0xc000
	ds_read_b128 v[198:201], v146
	ds_read_b128 v[202:205], v146 offset:1024
	ds_read_b128 v[206:209], v146 offset:2048
	ds_read_b128 v[210:213], v146 offset:3072
	ds_read_b128 v[214:217], v146 offset:4096
	ds_read_b128 v[218:221], v146 offset:5120
	ds_read_b128 v[222:225], v146 offset:6144
	ds_read_b128 v[226:229], v146 offset:7168
	global_load_lds_dwordx4 v114, s[44:45]
	s_add_i32 m0, s37, 0xe000
	s_nop 0
	global_load_lds_dwordx4 v142, s[44:45]
	s_waitcnt vmcnt(8)
	s_waitcnt lgkmcnt(0)
	s_barrier
	s_setprio 1
	s_waitcnt lgkmcnt(0)
	v_mfma_f32_16x16x32_bf16 v[2:5], v[148:151], v[198:201], v[2:5]
	v_mfma_f32_16x16x32_bf16 v[6:9], v[158:161], v[198:201], v[6:9]
	v_mfma_f32_16x16x32_bf16 v[10:13], v[148:151], v[206:209], v[10:13]
	v_mfma_f32_16x16x32_bf16 v[14:17], v[158:161], v[206:209], v[14:17]
	v_mfma_f32_16x16x32_bf16 v[26:29], v[148:151], v[214:217], v[26:29]
	v_mfma_f32_16x16x32_bf16 v[30:33], v[158:161], v[214:217], v[30:33]
	v_mfma_f32_16x16x32_bf16 v[42:45], v[148:151], v[222:225], v[42:45]
	v_mfma_f32_16x16x32_bf16 v[46:49], v[158:161], v[222:225], v[46:49]
	v_mfma_f32_16x16x32_bf16 v[2:5], v[152:155], v[202:205], v[2:5]
	v_mfma_f32_16x16x32_bf16 v[6:9], v[166:169], v[202:205], v[6:9]
	v_mfma_f32_16x16x32_bf16 v[10:13], v[152:155], v[210:213], v[10:13]
	v_mfma_f32_16x16x32_bf16 v[14:17], v[166:169], v[210:213], v[14:17]
	v_mfma_f32_16x16x32_bf16 v[26:29], v[152:155], v[218:221], v[26:29]
	v_mfma_f32_16x16x32_bf16 v[30:33], v[166:169], v[218:221], v[30:33]
	v_mfma_f32_16x16x32_bf16 v[42:45], v[152:155], v[226:229], v[42:45]
	v_mfma_f32_16x16x32_bf16 v[46:49], v[166:169], v[226:229], v[46:49]
	s_setprio 0
	s_setprio 1
	v_mfma_f32_16x16x32_bf16 v[18:21], v[170:173], v[198:201], v[18:21]
	v_mfma_f32_16x16x32_bf16 v[22:25], v[178:181], v[198:201], v[22:25]
	v_mfma_f32_16x16x32_bf16 v[34:37], v[170:173], v[206:209], v[34:37]
	v_mfma_f32_16x16x32_bf16 v[38:41], v[178:181], v[206:209], v[38:41]
	v_mfma_f32_16x16x32_bf16 v[50:53], v[170:173], v[214:217], v[50:53]
	v_mfma_f32_16x16x32_bf16 v[54:57], v[178:181], v[214:217], v[54:57]
	v_mfma_f32_16x16x32_bf16 v[58:61], v[170:173], v[222:225], v[58:61]
	v_mfma_f32_16x16x32_bf16 v[62:65], v[178:181], v[222:225], v[62:65]
	v_mfma_f32_16x16x32_bf16 v[18:21], v[174:177], v[202:205], v[18:21]
	v_mfma_f32_16x16x32_bf16 v[22:25], v[194:197], v[202:205], v[22:25]
	v_mfma_f32_16x16x32_bf16 v[34:37], v[174:177], v[210:213], v[34:37]
	v_mfma_f32_16x16x32_bf16 v[38:41], v[194:197], v[210:213], v[38:41]
	v_mfma_f32_16x16x32_bf16 v[50:53], v[174:177], v[218:221], v[50:53]
	v_mfma_f32_16x16x32_bf16 v[54:57], v[194:197], v[218:221], v[54:57]
	v_mfma_f32_16x16x32_bf16 v[58:61], v[174:177], v[226:229], v[58:61]
	v_mfma_f32_16x16x32_bf16 v[62:65], v[194:197], v[226:229], v[62:65]
	s_setprio 0
	s_barrier
	s_add_i32 s16, s16, s24
	s_mov_b32 m0, s16
	ds_read_b128 v[198:201], v146 offset:16384
	ds_read_b128 v[202:205], v146 offset:17408
	ds_read_b128 v[206:209], v146 offset:18432
	ds_read_b128 v[210:213], v146 offset:19456
	ds_read_b128 v[214:217], v146 offset:20480
	ds_read_b128 v[218:221], v146 offset:21504
	ds_read_b128 v[222:225], v146 offset:22528
	ds_read_b128 v[226:229], v146 offset:23552
	global_load_lds_dwordx4 v134, s[46:47]
	s_add_i32 m0, s16, 0x2000
	s_add_u32 s16, s46, 0x1000
	s_addc_u32 s17, s47, 0
	s_add_i32 s61, s61, s24
	global_load_lds_dwordx4 v138, s[46:47]
	s_mov_b32 m0, s61
	s_nop 0
	global_load_lds_dwordx4 v134, s[16:17]
	s_add_i32 m0, s61, 0x2000
	s_nop 0
	global_load_lds_dwordx4 v138, s[16:17]
	s_mov_b32 m0, s37
	s_nop 0
	global_load_lds_dwordx4 v132, s[48:49]
	s_mov_b32 m0, s50
	s_nop 0
	global_load_lds_dwordx4 v136, s[48:49]
	s_waitcnt vmcnt(8)
	s_waitcnt lgkmcnt(0)
	s_barrier
	s_setprio 1
	s_waitcnt lgkmcnt(0)
	v_mfma_f32_16x16x32_bf16 v[66:69], v[148:151], v[198:201], v[66:69]
	v_mfma_f32_16x16x32_bf16 v[70:73], v[158:161], v[198:201], v[70:73]
	v_mfma_f32_16x16x32_bf16 v[74:77], v[148:151], v[206:209], v[74:77]
	v_mfma_f32_16x16x32_bf16 v[78:81], v[158:161], v[206:209], v[78:81]
	v_mfma_f32_16x16x32_bf16 v[86:89], v[148:151], v[214:217], v[86:89]
	v_mfma_f32_16x16x32_bf16 v[94:97], v[158:161], v[214:217], v[94:97]
	v_mfma_f32_16x16x32_bf16 v[102:105], v[148:151], v[222:225], v[102:105]
	v_mfma_f32_16x16x32_bf16 v[110:113], v[158:161], v[222:225], v[110:113]
	v_mfma_f32_16x16x32_bf16 v[66:69], v[152:155], v[202:205], v[66:69]
	v_mfma_f32_16x16x32_bf16 v[70:73], v[166:169], v[202:205], v[70:73]
	v_mfma_f32_16x16x32_bf16 v[74:77], v[152:155], v[210:213], v[74:77]
	v_mfma_f32_16x16x32_bf16 v[78:81], v[166:169], v[210:213], v[78:81]
	v_mfma_f32_16x16x32_bf16 v[86:89], v[152:155], v[218:221], v[86:89]
	v_mfma_f32_16x16x32_bf16 v[94:97], v[166:169], v[218:221], v[94:97]
	v_mfma_f32_16x16x32_bf16 v[102:105], v[152:155], v[226:229], v[102:105]
	v_mfma_f32_16x16x32_bf16 v[110:113], v[166:169], v[226:229], v[110:113]
	s_setprio 0
	s_setprio 1
	v_mfma_f32_16x16x32_bf16 v[82:85], v[170:173], v[198:201], v[82:85]
	v_mfma_f32_16x16x32_bf16 v[90:93], v[178:181], v[198:201], v[90:93]
	v_mfma_f32_16x16x32_bf16 v[98:101], v[170:173], v[206:209], v[98:101]
	v_mfma_f32_16x16x32_bf16 v[106:109], v[178:181], v[206:209], v[106:109]
	v_mfma_f32_16x16x32_bf16 v[116:119], v[170:173], v[214:217], v[116:119]
	v_mfma_f32_16x16x32_bf16 v[120:123], v[178:181], v[214:217], v[120:123]
	v_mfma_f32_16x16x32_bf16 v[124:127], v[170:173], v[222:225], v[124:127]
	v_mfma_f32_16x16x32_bf16 v[128:131], v[178:181], v[222:225], v[128:131]
	v_mfma_f32_16x16x32_bf16 v[82:85], v[174:177], v[202:205], v[82:85]
	v_mfma_f32_16x16x32_bf16 v[90:93], v[194:197], v[202:205], v[90:93]
	v_mfma_f32_16x16x32_bf16 v[98:101], v[174:177], v[210:213], v[98:101]
	v_mfma_f32_16x16x32_bf16 v[106:109], v[194:197], v[210:213], v[106:109]
	v_mfma_f32_16x16x32_bf16 v[116:119], v[174:177], v[218:221], v[116:119]
	v_mfma_f32_16x16x32_bf16 v[120:123], v[194:197], v[218:221], v[120:123]
	v_mfma_f32_16x16x32_bf16 v[124:127], v[174:177], v[226:229], v[124:127]
	v_mfma_f32_16x16x32_bf16 v[128:131], v[194:197], v[226:229], v[128:131]
	s_setprio 0
	s_barrier
	s_add_i32 s61, 0, 0x18000
	v_add_u32_e32 v147, s61, v144
	s_add_i32 s62, 0, 0x1c000
	ds_read_b128 v[148:151], v147
	ds_read_b128 v[152:155], v147 offset:1024
	ds_read_b128 v[158:161], v147 offset:2048
	ds_read_b128 v[166:169], v147 offset:3072
	v_add_u32_e32 v147, s62, v144
	ds_read_b128 v[170:173], v147
	ds_read_b128 v[174:177], v147 offset:1024
	ds_read_b128 v[178:181], v147 offset:2048
	ds_read_b128 v[194:197], v147 offset:3072
	s_add_u32 s16, s48, 0x4000
	s_addc_u32 s17, s49, 0
	s_mov_b32 m0, s51
	ds_read_b128 v[198:201], v146 offset:32768
	ds_read_b128 v[202:205], v146 offset:33792
	ds_read_b128 v[206:209], v146 offset:34816
	ds_read_b128 v[210:213], v146 offset:35840
	ds_read_b128 v[214:217], v146 offset:36864
	ds_read_b128 v[218:221], v146 offset:37888
	ds_read_b128 v[222:225], v146 offset:38912
	ds_read_b128 v[226:229], v146 offset:39936
	global_load_lds_dwordx4 v132, s[16:17]
	s_mov_b32 m0, s52
	s_nop 0
	global_load_lds_dwordx4 v136, s[16:17]
	s_waitcnt vmcnt(8)
	s_waitcnt lgkmcnt(0)
	s_barrier
	s_setprio 1
	s_waitcnt lgkmcnt(0)
	v_mfma_f32_16x16x32_bf16 v[2:5], v[148:151], v[198:201], v[2:5]
	v_mfma_f32_16x16x32_bf16 v[6:9], v[158:161], v[198:201], v[6:9]
	v_mfma_f32_16x16x32_bf16 v[10:13], v[148:151], v[206:209], v[10:13]
	v_mfma_f32_16x16x32_bf16 v[14:17], v[158:161], v[206:209], v[14:17]
	v_mfma_f32_16x16x32_bf16 v[26:29], v[148:151], v[214:217], v[26:29]
	v_mfma_f32_16x16x32_bf16 v[30:33], v[158:161], v[214:217], v[30:33]
	v_mfma_f32_16x16x32_bf16 v[42:45], v[148:151], v[222:225], v[42:45]
	v_mfma_f32_16x16x32_bf16 v[46:49], v[158:161], v[222:225], v[46:49]
	v_mfma_f32_16x16x32_bf16 v[2:5], v[152:155], v[202:205], v[2:5]
	v_mfma_f32_16x16x32_bf16 v[6:9], v[166:169], v[202:205], v[6:9]
	v_mfma_f32_16x16x32_bf16 v[10:13], v[152:155], v[210:213], v[10:13]
	v_mfma_f32_16x16x32_bf16 v[14:17], v[166:169], v[210:213], v[14:17]
	v_mfma_f32_16x16x32_bf16 v[26:29], v[152:155], v[218:221], v[26:29]
	v_mfma_f32_16x16x32_bf16 v[30:33], v[166:169], v[218:221], v[30:33]
	v_mfma_f32_16x16x32_bf16 v[42:45], v[152:155], v[226:229], v[42:45]
	v_mfma_f32_16x16x32_bf16 v[46:49], v[166:169], v[226:229], v[46:49]
	s_setprio 0
	s_setprio 1
	v_mfma_f32_16x16x32_bf16 v[18:21], v[170:173], v[198:201], v[18:21]
	v_mfma_f32_16x16x32_bf16 v[22:25], v[178:181], v[198:201], v[22:25]
	v_mfma_f32_16x16x32_bf16 v[34:37], v[170:173], v[206:209], v[34:37]
	v_mfma_f32_16x16x32_bf16 v[38:41], v[178:181], v[206:209], v[38:41]
	v_mfma_f32_16x16x32_bf16 v[50:53], v[170:173], v[214:217], v[50:53]
	v_mfma_f32_16x16x32_bf16 v[54:57], v[178:181], v[214:217], v[54:57]
	v_mfma_f32_16x16x32_bf16 v[58:61], v[170:173], v[222:225], v[58:61]
	v_mfma_f32_16x16x32_bf16 v[62:65], v[178:181], v[222:225], v[62:65]
	v_mfma_f32_16x16x32_bf16 v[18:21], v[174:177], v[202:205], v[18:21]
	v_mfma_f32_16x16x32_bf16 v[22:25], v[194:197], v[202:205], v[22:25]
	v_mfma_f32_16x16x32_bf16 v[34:37], v[174:177], v[210:213], v[34:37]
	v_mfma_f32_16x16x32_bf16 v[38:41], v[194:197], v[210:213], v[38:41]
	v_mfma_f32_16x16x32_bf16 v[50:53], v[174:177], v[218:221], v[50:53]
	v_mfma_f32_16x16x32_bf16 v[54:57], v[194:197], v[218:221], v[54:57]
	v_mfma_f32_16x16x32_bf16 v[58:61], v[174:177], v[226:229], v[58:61]
	v_mfma_f32_16x16x32_bf16 v[62:65], v[194:197], v[226:229], v[62:65]
	s_setprio 0
	s_barrier
	s_add_u32 s16, s46, 0x8000
	s_addc_u32 s17, s47, 0
	s_add_i32 s48, s61, s24
	s_mov_b32 m0, s48
	ds_read_b128 v[198:201], v146 offset:49152
	ds_read_b128 v[202:205], v146 offset:50176
	ds_read_b128 v[206:209], v146 offset:51200
	ds_read_b128 v[210:213], v146 offset:52224
	ds_read_b128 v[214:217], v146 offset:53248
	ds_read_b128 v[218:221], v146 offset:54272
	ds_read_b128 v[222:225], v146 offset:55296
	ds_read_b128 v[226:229], v146 offset:56320
	global_load_lds_dwordx4 v134, s[16:17]
	s_add_i32 m0, s48, 0x2000
	v_lshl_add_u64 v[182:183], s[16:17], 0, v[138:139]
	s_add_u32 s16, s46, 0x9000
	s_addc_u32 s17, s47, 0
	s_add_i32 s46, s62, s24
	global_load_lds_dwordx4 v[182:183], off
	s_mov_b32 m0, s46
	s_nop 0
	global_load_lds_dwordx4 v134, s[16:17]
	s_add_i32 m0, s46, 0x2000
	s_nop 0
	global_load_lds_dwordx4 v138, s[16:17]
	s_mov_b32 m0, s53
	s_nop 0
	global_load_lds_dwordx4 v132, s[42:43]
	s_mov_b32 m0, s54
	s_nop 0
	global_load_lds_dwordx4 v136, s[42:43]
	s_waitcnt vmcnt(8)
	s_waitcnt lgkmcnt(0)
	s_barrier
	s_setprio 1
	s_waitcnt lgkmcnt(0)
	v_mfma_f32_16x16x32_bf16 v[66:69], v[148:151], v[198:201], v[66:69]
	v_mfma_f32_16x16x32_bf16 v[70:73], v[158:161], v[198:201], v[70:73]
	v_mfma_f32_16x16x32_bf16 v[74:77], v[148:151], v[206:209], v[74:77]
	v_mfma_f32_16x16x32_bf16 v[78:81], v[158:161], v[206:209], v[78:81]
	v_mfma_f32_16x16x32_bf16 v[86:89], v[148:151], v[214:217], v[86:89]
	v_mfma_f32_16x16x32_bf16 v[94:97], v[158:161], v[214:217], v[94:97]
	v_mfma_f32_16x16x32_bf16 v[102:105], v[148:151], v[222:225], v[102:105]
	v_mfma_f32_16x16x32_bf16 v[110:113], v[158:161], v[222:225], v[110:113]
	v_mfma_f32_16x16x32_bf16 v[66:69], v[152:155], v[202:205], v[66:69]
	v_mfma_f32_16x16x32_bf16 v[70:73], v[166:169], v[202:205], v[70:73]
	v_mfma_f32_16x16x32_bf16 v[74:77], v[152:155], v[210:213], v[74:77]
	v_mfma_f32_16x16x32_bf16 v[78:81], v[166:169], v[210:213], v[78:81]
	v_mfma_f32_16x16x32_bf16 v[86:89], v[152:155], v[218:221], v[86:89]
	v_mfma_f32_16x16x32_bf16 v[94:97], v[166:169], v[218:221], v[94:97]
	v_mfma_f32_16x16x32_bf16 v[102:105], v[152:155], v[226:229], v[102:105]
	v_mfma_f32_16x16x32_bf16 v[110:113], v[166:169], v[226:229], v[110:113]
	s_setprio 0
	s_setprio 1
	v_mfma_f32_16x16x32_bf16 v[82:85], v[170:173], v[198:201], v[82:85]
	v_mfma_f32_16x16x32_bf16 v[90:93], v[178:181], v[198:201], v[90:93]
	v_mfma_f32_16x16x32_bf16 v[98:101], v[170:173], v[206:209], v[98:101]
	v_mfma_f32_16x16x32_bf16 v[106:109], v[178:181], v[206:209], v[106:109]
	v_mfma_f32_16x16x32_bf16 v[116:119], v[170:173], v[214:217], v[116:119]
	v_mfma_f32_16x16x32_bf16 v[120:123], v[178:181], v[214:217], v[120:123]
	v_mfma_f32_16x16x32_bf16 v[124:127], v[170:173], v[222:225], v[124:127]
	v_mfma_f32_16x16x32_bf16 v[128:131], v[178:181], v[222:225], v[128:131]
	v_mfma_f32_16x16x32_bf16 v[82:85], v[174:177], v[202:205], v[82:85]
	v_mfma_f32_16x16x32_bf16 v[90:93], v[194:197], v[202:205], v[90:93]
	v_mfma_f32_16x16x32_bf16 v[98:101], v[174:177], v[210:213], v[98:101]
	v_mfma_f32_16x16x32_bf16 v[106:109], v[194:197], v[210:213], v[106:109]
	v_mfma_f32_16x16x32_bf16 v[116:119], v[174:177], v[218:221], v[116:119]
	v_mfma_f32_16x16x32_bf16 v[120:123], v[194:197], v[218:221], v[120:123]
	v_mfma_f32_16x16x32_bf16 v[124:127], v[174:177], v[226:229], v[124:127]
	v_mfma_f32_16x16x32_bf16 v[128:131], v[194:197], v[226:229], v[128:131]
	s_setprio 0
	s_barrier
	s_add_i32 s60, s60, 2
	s_add_u32 s44, s44, 0x10000
	s_addc_u32 s45, s45, 0
	s_add_u32 s58, s58, 0x10000
	s_addc_u32 s59, s59, 0
	s_cmpk_gt_u32 s60, 0x7d
	s_cbranch_scc0 .LBB0_1376
	s_and_b64 vcc, exec, s[8:9]
	s_cbranch_vccz .LBB0_1379
	s_barrier
